# baseline (speedup 1.0000x reference)
.Lrs_a_4:
	s_add_u32 s81, s40, s22
	s_addc_u32 s82, s41, s23
	s_add_u32 s29, s40, 0x100
	s_addc_u32 s44, s41, 0
	s_and_b64 s[42:43], s[14:15], exec
	ds_read_b128 v[82:85], v161
	ds_read_b128 v[94:97], v161 offset:2048
	ds_read_b128 v[102:105], v162
	ds_read_b128 v[110:113], v162 offset:2048
	s_cselect_b32 s47, s37, s44
	s_cselect_b32 s46, s36, s29
	s_add_u32 s29, s38, 0x100
	s_addc_u32 s44, s39, 0
	s_and_b64 s[42:43], s[14:15], exec
	s_cselect_b32 s49, s5, s44
	s_cselect_b32 s48, s4, s29
	s_add_u32 s44, s46, 0x80
	s_addc_u32 s45, s47, 0
	s_add_u32 s42, s48, 0x80
	s_addc_u32 s43, s49, 0
	ds_read_b128 v[58:61], v163
	ds_read_b128 v[66:69], v163 offset:2048
	ds_read_b128 v[62:65], v164
	ds_read_b128 v[70:73], v164 offset:2048
	ds_read_b128 v[74:77], v163 offset:4096
	ds_read_b128 v[86:89], v163 offset:6144
	ds_read_b128 v[78:81], v164 offset:4096
	ds_read_b128 v[90:93], v164 offset:6144
	s_add_u32 s78, s81, 0x80
	s_addc_u32 s79, s82, 0
	s_mov_b32 m0, s70
	s_nop 0
	global_load_lds_dwordx4 v146, s[78:79]
	s_mov_b32 m0, s71
	s_nop 0
	global_load_lds_dwordx4 v150, s[78:79]
	s_waitcnt lgkmcnt(8)
	ds_read_b128 v[142:145], v161 offset:16384
	ds_read_b128 v[166:169], v161 offset:18432
	ds_read_b128 v[170:173], v162 offset:16384
	ds_read_b128 v[174:177], v162 offset:18432
	s_waitcnt vmcnt(8)
	s_waitcnt lgkmcnt(0)
	s_barrier
	s_waitcnt lgkmcnt(0)
	s_waitcnt vmcnt(16)
	v_mov_b32_e32 v1, v0
	v_pk_mul_f32 v[16:17], v[0:1], v[16:17]
	v_pk_mul_f32 v[14:15], v[154:155], v[14:15]
	v_pk_mul_f32 v[12:13], v[0:1], v[12:13]
	v_pk_mul_f32 v[10:11], v[154:155], v[10:11]
	v_pk_mul_f32 v[8:9], v[0:1], v[8:9]
	v_pk_mul_f32 v[6:7], v[154:155], v[6:7]
	v_pk_mul_f32 v[4:5], v[0:1], v[4:5]
	v_pk_mul_f32 v[2:3], v[154:155], v[2:3]
	v_mfma_f32_16x16x128_f8f6f4 v[18:21], v[82:85], v[58:61], v[14:17] cbsz:4 blgp:4
	v_mfma_f32_16x16x128_f8f6f4 v[18:21], v[102:105], v[62:65], v[18:21] cbsz:4 blgp:4
	v_mfma_f32_16x16x128_f8f6f4 v[22:25], v[94:97], v[58:61], v[10:13] cbsz:4 blgp:4
	v_mfma_f32_16x16x128_f8f6f4 v[22:25], v[110:113], v[62:65], v[22:25] cbsz:4 blgp:4
	v_mfma_f32_16x16x128_f8f6f4 v[26:29], v[82:85], v[66:69], v[14:17] cbsz:4 blgp:4
	v_mfma_f32_16x16x128_f8f6f4 v[26:29], v[102:105], v[70:73], v[26:29] cbsz:4 blgp:4
	v_mfma_f32_16x16x128_f8f6f4 v[30:33], v[94:97], v[66:69], v[10:13] cbsz:4 blgp:4
	v_mfma_f32_16x16x128_f8f6f4 v[30:33], v[110:113], v[70:73], v[30:33] cbsz:4 blgp:4
	v_mfma_f32_16x16x128_f8f6f4 v[34:37], v[82:85], v[74:77], v[14:17] cbsz:4 blgp:4
	v_mfma_f32_16x16x128_f8f6f4 v[34:37], v[102:105], v[78:81], v[34:37] cbsz:4 blgp:4
	v_mfma_f32_16x16x128_f8f6f4 v[38:41], v[94:97], v[74:77], v[10:13] cbsz:4 blgp:4
	v_mfma_f32_16x16x128_f8f6f4 v[38:41], v[110:113], v[78:81], v[38:41] cbsz:4 blgp:4
	v_mfma_f32_16x16x128_f8f6f4 v[42:45], v[82:85], v[86:89], v[14:17] cbsz:4 blgp:4
	v_mfma_f32_16x16x128_f8f6f4 v[42:45], v[102:105], v[90:93], v[42:45] cbsz:4 blgp:4
	v_mfma_f32_16x16x128_f8f6f4 v[46:49], v[94:97], v[86:89], v[10:13] cbsz:4 blgp:4
	v_mfma_f32_16x16x128_f8f6f4 v[46:49], v[110:113], v[90:93], v[46:49] cbsz:4 blgp:4
	v_mfma_f32_16x16x128_f8f6f4 v[50:53], v[142:145], v[58:61], v[6:9] cbsz:4 blgp:4
	v_mfma_f32_16x16x128_f8f6f4 v[50:53], v[170:173], v[62:65], v[50:53] cbsz:4 blgp:4
	v_mfma_f32_16x16x128_f8f6f4 v[54:57], v[166:169], v[58:61], v[2:5] cbsz:4 blgp:4
	v_mfma_f32_16x16x128_f8f6f4 v[54:57], v[174:177], v[62:65], v[54:57] cbsz:4 blgp:4
	v_mfma_f32_16x16x128_f8f6f4 v[58:61], v[142:145], v[66:69], v[6:9] cbsz:4 blgp:4
	v_mfma_f32_16x16x128_f8f6f4 v[58:61], v[170:173], v[70:73], v[58:61] cbsz:4 blgp:4
	v_mfma_f32_16x16x128_f8f6f4 v[62:65], v[166:169], v[66:69], v[2:5] cbsz:4 blgp:4
	v_mfma_f32_16x16x128_f8f6f4 v[62:65], v[174:177], v[70:73], v[62:65] cbsz:4 blgp:4
	v_mfma_f32_16x16x128_f8f6f4 v[66:69], v[142:145], v[74:77], v[6:9] cbsz:4 blgp:4
	v_mfma_f32_16x16x128_f8f6f4 v[66:69], v[170:173], v[78:81], v[66:69] cbsz:4 blgp:4
	v_mfma_f32_16x16x128_f8f6f4 v[70:73], v[166:169], v[74:77], v[2:5] cbsz:4 blgp:4
	v_mfma_f32_16x16x128_f8f6f4 v[70:73], v[174:177], v[78:81], v[70:73] cbsz:4 blgp:4
	v_mfma_f32_16x16x128_f8f6f4 v[74:77], v[142:145], v[86:89], v[6:9] cbsz:4 blgp:4
	v_mfma_f32_16x16x128_f8f6f4 v[74:77], v[170:173], v[90:93], v[74:77] cbsz:4 blgp:4
	v_mfma_f32_16x16x128_f8f6f4 v[78:81], v[166:169], v[86:89], v[2:5] cbsz:4 blgp:4
	v_mfma_f32_16x16x128_f8f6f4 v[78:81], v[174:177], v[90:93], v[78:81] cbsz:4 blgp:4
	s_barrier
	s_mov_b32 m0, s55
	s_nop 0
	global_load_lds_dwordx4 v148, s[48:49]
	s_mov_b32 m0, s56
	s_nop 0
	global_load_lds_dwordx4 v152, s[48:49]
	ds_read_b128 v[114:117], v163 offset:16384
	ds_read_b128 v[122:125], v163 offset:18432
	ds_read_b128 v[130:133], v164 offset:16384
	ds_read_b128 v[134:137], v164 offset:18432
	ds_read_b128 v[178:181], v163 offset:20480
	ds_read_b128 v[182:185], v163 offset:22528
	ds_read_b128 v[186:189], v164 offset:20480
	ds_read_b128 v[190:193], v164 offset:22528
	s_mov_b32 m0, s54
	s_nop 0
	global_load_lds_dwordx4 v146, s[46:47]
	s_mov_b32 m0, s57
	s_nop 0
	global_load_lds_dwordx4 v150, s[46:47]
	s_add_u32 s48, s48, s24
	s_addc_u32 s49, s49, s25
	s_mov_b32 m0, s58
	s_nop 0
	global_load_lds_dwordx4 v148, s[48:49]
	s_mov_b32 m0, s59
	s_nop 0
	global_load_lds_dwordx4 v152, s[48:49]
	s_waitcnt vmcnt(8)
	s_waitcnt lgkmcnt(0)
	s_barrier
	v_mfma_f32_16x16x128_f8f6f4 v[86:89], v[82:85], v[114:117], v[14:17] cbsz:4 blgp:4
	v_mfma_f32_16x16x128_f8f6f4 v[86:89], v[102:105], v[130:133], v[86:89] cbsz:4 blgp:4
	v_mfma_f32_16x16x128_f8f6f4 v[90:93], v[94:97], v[114:117], v[10:13] cbsz:4 blgp:4
	v_mfma_f32_16x16x128_f8f6f4 v[90:93], v[110:113], v[130:133], v[90:93] cbsz:4 blgp:4
	v_mfma_f32_16x16x128_f8f6f4 v[98:101], v[82:85], v[122:125], v[14:17] cbsz:4 blgp:4
	v_mfma_f32_16x16x128_f8f6f4 v[98:101], v[102:105], v[134:137], v[98:101] cbsz:4 blgp:4
	v_mfma_f32_16x16x128_f8f6f4 v[106:109], v[94:97], v[122:125], v[10:13] cbsz:4 blgp:4
	v_mfma_f32_16x16x128_f8f6f4 v[106:109], v[110:113], v[134:137], v[106:109] cbsz:4 blgp:4
	v_mfma_f32_16x16x128_f8f6f4 v[118:121], v[82:85], v[178:181], v[14:17] cbsz:4 blgp:4
	v_mfma_f32_16x16x128_f8f6f4 v[118:121], v[102:105], v[186:189], v[118:121] cbsz:4 blgp:4
	v_mfma_f32_16x16x128_f8f6f4 v[126:129], v[94:97], v[178:181], v[10:13] cbsz:4 blgp:4
	v_mfma_f32_16x16x128_f8f6f4 v[126:129], v[110:113], v[186:189], v[126:129] cbsz:4 blgp:4
	v_mfma_f32_16x16x128_f8f6f4 v[138:141], v[82:85], v[182:185], v[14:17] cbsz:4 blgp:4
	v_mfma_f32_16x16x128_f8f6f4 v[138:141], v[102:105], v[190:193], v[138:141] cbsz:4 blgp:4
	v_mfma_f32_16x16x128_f8f6f4 v[82:85], v[94:97], v[182:185], v[10:13] cbsz:4 blgp:4
	v_mfma_f32_16x16x128_f8f6f4 v[82:85], v[110:113], v[190:193], v[82:85] cbsz:4 blgp:4
	v_mfma_f32_16x16x128_f8f6f4 v[94:97], v[142:145], v[114:117], v[6:9] cbsz:4 blgp:4
	v_mfma_f32_16x16x128_f8f6f4 v[94:97], v[170:173], v[130:133], v[94:97] cbsz:4 blgp:4
	v_mfma_f32_16x16x128_f8f6f4 v[102:105], v[166:169], v[114:117], v[2:5] cbsz:4 blgp:4
	v_mfma_f32_16x16x128_f8f6f4 v[102:105], v[174:177], v[130:133], v[102:105] cbsz:4 blgp:4
	v_mfma_f32_16x16x128_f8f6f4 v[110:113], v[142:145], v[122:125], v[6:9] cbsz:4 blgp:4
	v_mfma_f32_16x16x128_f8f6f4 v[110:113], v[170:173], v[134:137], v[110:113] cbsz:4 blgp:4
	v_mfma_f32_16x16x128_f8f6f4 v[114:117], v[166:169], v[122:125], v[2:5] cbsz:4 blgp:4
	v_mfma_f32_16x16x128_f8f6f4 v[114:117], v[174:177], v[134:137], v[114:117] cbsz:4 blgp:4
	v_mfma_f32_16x16x128_f8f6f4 v[122:125], v[142:145], v[178:181], v[6:9] cbsz:4 blgp:4
	v_mfma_f32_16x16x128_f8f6f4 v[122:125], v[170:173], v[186:189], v[122:125] cbsz:4 blgp:4
	v_mfma_f32_16x16x128_f8f6f4 v[130:133], v[166:169], v[178:181], v[2:5] cbsz:4 blgp:4
	v_mfma_f32_16x16x128_f8f6f4 v[130:133], v[174:177], v[186:189], v[130:133] cbsz:4 blgp:4
	v_mfma_f32_16x16x128_f8f6f4 v[134:137], v[142:145], v[182:185], v[6:9] cbsz:4 blgp:4
	v_mfma_f32_16x16x128_f8f6f4 v[134:137], v[170:173], v[190:193], v[134:137] cbsz:4 blgp:4
	v_mfma_f32_16x16x128_f8f6f4 v[142:145], v[166:169], v[182:185], v[2:5] cbsz:4 blgp:4
	v_mfma_f32_16x16x128_f8f6f4 v[142:145], v[174:177], v[190:193], v[142:145] cbsz:4 blgp:4
	s_barrier
	ds_read_b128 v[166:169], v161 offset:32768
	ds_read_b128 v[170:173], v161 offset:34816
	ds_read_b128 v[174:177], v162 offset:32768
	ds_read_b128 v[178:181], v162 offset:34816
	ds_read_b128 v[182:185], v163 offset:32768
	ds_read_b128 v[186:189], v163 offset:34816
	ds_read_b128 v[190:193], v164 offset:32768
	ds_read_b128 v[194:197], v164 offset:34816
	ds_read_b128 v[198:201], v163 offset:36864
	ds_read_b128 v[202:205], v163 offset:38912
	ds_read_b128 v[206:209], v164 offset:36864
	ds_read_b128 v[210:213], v164 offset:38912
	s_add_u32 s46, s46, s22
	s_addc_u32 s47, s47, s23
	s_mov_b32 m0, s60
	s_nop 0
	global_load_lds_dwordx4 v146, s[46:47]
	s_mov_b32 m0, s61
	s_nop 0
	global_load_lds_dwordx4 v150, s[46:47]
	s_waitcnt lgkmcnt(8)
	ds_read_b128 v[214:217], v161 offset:49152
	ds_read_b128 v[218:221], v161 offset:51200
	ds_read_b128 v[222:225], v162 offset:49152
	ds_read_b128 v[226:229], v162 offset:51200
	s_waitcnt vmcnt(8)
	s_waitcnt lgkmcnt(0)
	s_barrier
	s_waitcnt lgkmcnt(0)
	v_mfma_f32_16x16x128_f8f6f4 v[18:21], v[166:169], v[182:185], v[18:21] cbsz:4 blgp:4
	v_mfma_f32_16x16x128_f8f6f4 v[18:21], v[174:177], v[190:193], v[18:21] cbsz:4 blgp:4
	v_mfma_f32_16x16x128_f8f6f4 v[22:25], v[170:173], v[182:185], v[22:25] cbsz:4 blgp:4
	v_mfma_f32_16x16x128_f8f6f4 v[22:25], v[178:181], v[190:193], v[22:25] cbsz:4 blgp:4
	v_mfma_f32_16x16x128_f8f6f4 v[26:29], v[166:169], v[186:189], v[26:29] cbsz:4 blgp:4
	v_mfma_f32_16x16x128_f8f6f4 v[26:29], v[174:177], v[194:197], v[26:29] cbsz:4 blgp:4
	v_mfma_f32_16x16x128_f8f6f4 v[30:33], v[170:173], v[186:189], v[30:33] cbsz:4 blgp:4
	v_mfma_f32_16x16x128_f8f6f4 v[30:33], v[178:181], v[194:197], v[30:33] cbsz:4 blgp:4
	v_mfma_f32_16x16x128_f8f6f4 v[34:37], v[166:169], v[198:201], v[34:37] cbsz:4 blgp:4
	v_mfma_f32_16x16x128_f8f6f4 v[34:37], v[174:177], v[206:209], v[34:37] cbsz:4 blgp:4
	v_mfma_f32_16x16x128_f8f6f4 v[38:41], v[170:173], v[198:201], v[38:41] cbsz:4 blgp:4
	v_mfma_f32_16x16x128_f8f6f4 v[38:41], v[178:181], v[206:209], v[38:41] cbsz:4 blgp:4
	v_mfma_f32_16x16x128_f8f6f4 v[42:45], v[166:169], v[202:205], v[42:45] cbsz:4 blgp:4
	v_mfma_f32_16x16x128_f8f6f4 v[42:45], v[174:177], v[210:213], v[42:45] cbsz:4 blgp:4
	v_mfma_f32_16x16x128_f8f6f4 v[46:49], v[170:173], v[202:205], v[46:49] cbsz:4 blgp:4
	v_mfma_f32_16x16x128_f8f6f4 v[46:49], v[178:181], v[210:213], v[46:49] cbsz:4 blgp:4
	v_mfma_f32_16x16x128_f8f6f4 v[50:53], v[214:217], v[182:185], v[50:53] cbsz:4 blgp:4
	v_mfma_f32_16x16x128_f8f6f4 v[50:53], v[222:225], v[190:193], v[50:53] cbsz:4 blgp:4
	v_mfma_f32_16x16x128_f8f6f4 v[54:57], v[218:221], v[182:185], v[54:57] cbsz:4 blgp:4
	v_mfma_f32_16x16x128_f8f6f4 v[54:57], v[226:229], v[190:193], v[54:57] cbsz:4 blgp:4
	v_mfma_f32_16x16x128_f8f6f4 v[58:61], v[214:217], v[186:189], v[58:61] cbsz:4 blgp:4
	v_mfma_f32_16x16x128_f8f6f4 v[58:61], v[222:225], v[194:197], v[58:61] cbsz:4 blgp:4
	v_mfma_f32_16x16x128_f8f6f4 v[62:65], v[218:221], v[186:189], v[62:65] cbsz:4 blgp:4
	v_mfma_f32_16x16x128_f8f6f4 v[62:65], v[226:229], v[194:197], v[62:65] cbsz:4 blgp:4
	v_mfma_f32_16x16x128_f8f6f4 v[66:69], v[214:217], v[198:201], v[66:69] cbsz:4 blgp:4
	v_mfma_f32_16x16x128_f8f6f4 v[66:69], v[222:225], v[206:209], v[66:69] cbsz:4 blgp:4
	v_mfma_f32_16x16x128_f8f6f4 v[70:73], v[218:221], v[198:201], v[70:73] cbsz:4 blgp:4
	v_mfma_f32_16x16x128_f8f6f4 v[70:73], v[226:229], v[206:209], v[70:73] cbsz:4 blgp:4
	v_mfma_f32_16x16x128_f8f6f4 v[74:77], v[214:217], v[202:205], v[74:77] cbsz:4 blgp:4
	v_mfma_f32_16x16x128_f8f6f4 v[74:77], v[222:225], v[210:213], v[74:77] cbsz:4 blgp:4
	v_mfma_f32_16x16x128_f8f6f4 v[78:81], v[218:221], v[202:205], v[78:81] cbsz:4 blgp:4
	v_mfma_f32_16x16x128_f8f6f4 v[78:81], v[226:229], v[210:213], v[78:81] cbsz:4 blgp:4
	s_barrier
	s_mov_b32 m0, s64
	s_nop 0
	global_load_lds_dwordx4 v148, s[42:43]
	s_mov_b32 m0, s65
	s_nop 0
	global_load_lds_dwordx4 v152, s[42:43]
	ds_read_b128 v[182:185], v163 offset:49152
	ds_read_b128 v[186:189], v163 offset:51200
	ds_read_b128 v[190:193], v164 offset:49152
	ds_read_b128 v[194:197], v164 offset:51200
	ds_read_b128 v[198:201], v163 offset:53248
	ds_read_b128 v[202:205], v163 offset:55296
	ds_read_b128 v[206:209], v164 offset:53248
	ds_read_b128 v[210:213], v164 offset:55296
	s_mov_b32 m0, s66
	s_nop 0
	global_load_lds_dwordx4 v146, s[44:45]
	s_mov_b32 m0, s67
	s_nop 0
	global_load_lds_dwordx4 v150, s[44:45]
	s_add_u32 s42, s42, s24
	s_addc_u32 s43, s43, s25
	s_mov_b32 m0, s68
	s_nop 0
	global_load_lds_dwordx4 v148, s[42:43]
	s_mov_b32 m0, s69
	s_nop 0
	global_load_lds_dwordx4 v152, s[42:43]
	s_waitcnt vmcnt(8)
	s_waitcnt lgkmcnt(0)
	s_barrier
	v_mfma_f32_16x16x128_f8f6f4 v[86:89], v[166:169], v[182:185], v[86:89] cbsz:4 blgp:4
	v_mfma_f32_16x16x128_f8f6f4 v[86:89], v[174:177], v[190:193], v[86:89] cbsz:4 blgp:4
	v_mfma_f32_16x16x128_f8f6f4 v[90:93], v[170:173], v[182:185], v[90:93] cbsz:4 blgp:4
	v_mfma_f32_16x16x128_f8f6f4 v[90:93], v[178:181], v[190:193], v[90:93] cbsz:4 blgp:4
	v_mfma_f32_16x16x128_f8f6f4 v[98:101], v[166:169], v[186:189], v[98:101] cbsz:4 blgp:4
	v_mfma_f32_16x16x128_f8f6f4 v[98:101], v[174:177], v[194:197], v[98:101] cbsz:4 blgp:4
	v_mfma_f32_16x16x128_f8f6f4 v[106:109], v[170:173], v[186:189], v[106:109] cbsz:4 blgp:4
	v_mfma_f32_16x16x128_f8f6f4 v[106:109], v[178:181], v[194:197], v[106:109] cbsz:4 blgp:4
	v_mfma_f32_16x16x128_f8f6f4 v[118:121], v[166:169], v[198:201], v[118:121] cbsz:4 blgp:4
	v_mfma_f32_16x16x128_f8f6f4 v[118:121], v[174:177], v[206:209], v[118:121] cbsz:4 blgp:4
	v_mfma_f32_16x16x128_f8f6f4 v[126:129], v[170:173], v[198:201], v[126:129] cbsz:4 blgp:4
	v_mfma_f32_16x16x128_f8f6f4 v[126:129], v[178:181], v[206:209], v[126:129] cbsz:4 blgp:4
	v_mfma_f32_16x16x128_f8f6f4 v[138:141], v[166:169], v[202:205], v[138:141] cbsz:4 blgp:4
	v_mfma_f32_16x16x128_f8f6f4 v[138:141], v[174:177], v[210:213], v[138:141] cbsz:4 blgp:4
	v_mfma_f32_16x16x128_f8f6f4 v[82:85], v[170:173], v[202:205], v[82:85] cbsz:4 blgp:4
	v_mfma_f32_16x16x128_f8f6f4 v[82:85], v[178:181], v[210:213], v[82:85] cbsz:4 blgp:4
	v_mfma_f32_16x16x128_f8f6f4 v[94:97], v[214:217], v[182:185], v[94:97] cbsz:4 blgp:4
	v_mfma_f32_16x16x128_f8f6f4 v[94:97], v[222:225], v[190:193], v[94:97] cbsz:4 blgp:4
	v_mfma_f32_16x16x128_f8f6f4 v[102:105], v[218:221], v[182:185], v[102:105] cbsz:4 blgp:4
	v_mfma_f32_16x16x128_f8f6f4 v[102:105], v[226:229], v[190:193], v[102:105] cbsz:4 blgp:4
	v_mfma_f32_16x16x128_f8f6f4 v[110:113], v[214:217], v[186:189], v[110:113] cbsz:4 blgp:4
	v_mfma_f32_16x16x128_f8f6f4 v[110:113], v[222:225], v[194:197], v[110:113] cbsz:4 blgp:4
	v_mfma_f32_16x16x128_f8f6f4 v[114:117], v[218:221], v[186:189], v[114:117] cbsz:4 blgp:4
	v_mfma_f32_16x16x128_f8f6f4 v[114:117], v[226:229], v[194:197], v[114:117] cbsz:4 blgp:4
	v_mfma_f32_16x16x128_f8f6f4 v[122:125], v[214:217], v[198:201], v[122:125] cbsz:4 blgp:4
	v_mfma_f32_16x16x128_f8f6f4 v[122:125], v[222:225], v[206:209], v[122:125] cbsz:4 blgp:4
	v_mfma_f32_16x16x128_f8f6f4 v[130:133], v[218:221], v[198:201], v[130:133] cbsz:4 blgp:4
	v_mfma_f32_16x16x128_f8f6f4 v[130:133], v[226:229], v[206:209], v[130:133] cbsz:4 blgp:4
	v_mfma_f32_16x16x128_f8f6f4 v[134:137], v[214:217], v[202:205], v[134:137] cbsz:4 blgp:4
	v_mfma_f32_16x16x128_f8f6f4 v[134:137], v[222:225], v[210:213], v[134:137] cbsz:4 blgp:4
	v_mfma_f32_16x16x128_f8f6f4 v[142:145], v[218:221], v[202:205], v[142:145] cbsz:4 blgp:4
	v_mfma_f32_16x16x128_f8f6f4 v[142:145], v[226:229], v[210:213], v[142:145] cbsz:4 blgp:4
	s_andn2_b64 vcc, exec, s[34:35]
	s_barrier
	s_cbranch_vccnz .LBB4_4
	s_ashr_i32 s29, s28, 31
	s_lshl_b64 s[42:43], s[28:29], 10
	s_add_u32 s42, s10, s42
	s_addc_u32 s43, s11, s43
	s_add_u32 s29, s40, 0x200
	s_addc_u32 s78, s41, 0
	s_add_u32 s79, s38, 0x200
	s_addc_u32 s80, s39, 0
	s_add_u32 s38, s81, 0x180
	s_addc_u32 s39, s82, 0
	s_mov_b32 s81, 4
	s_cmp_eq_u32 s63, s81
	s_cselect_b64 s[40:41], -1, 0
	s_cmp_lg_u32 s63, s81
	s_cbranch_scc1 .LBB4_15

.LBB4_15:
	ds_read_b128 v[166:169], v161
	ds_read_b128 v[170:173], v161 offset:2048
	ds_read_b128 v[174:177], v162
	ds_read_b128 v[178:181], v162 offset:2048
	s_and_b64 s[40:41], s[40:41], exec
	s_cselect_b32 s46, s36, s29
	s_cselect_b32 s47, s37, s78
	s_cselect_b32 s49, s5, s80
	s_cselect_b32 s48, s4, s79
	s_add_u32 s44, s46, 0x80
	s_addc_u32 s45, s47, 0
	s_add_u32 s40, s48, 0x80
	s_addc_u32 s41, s49, 0
	ds_read_b128 v[182:185], v163
	ds_read_b128 v[186:189], v163 offset:2048
	ds_read_b128 v[190:193], v164
	ds_read_b128 v[194:197], v164 offset:2048
	ds_read_b128 v[198:201], v163 offset:4096
	ds_read_b128 v[202:205], v163 offset:6144
	ds_read_b128 v[206:209], v164 offset:4096
	ds_read_b128 v[210:213], v164 offset:6144
	s_mov_b32 m0, s70
	s_nop 0
	global_load_lds_dwordx4 v146, s[38:39]
	s_mov_b32 m0, s71
	s_nop 0
	global_load_lds_dwordx4 v150, s[38:39]
	s_waitcnt lgkmcnt(8)
	ds_read_b128 v[214:217], v161 offset:16384
	ds_read_b128 v[218:221], v161 offset:18432
	ds_read_b128 v[222:225], v162 offset:16384
	ds_read_b128 v[226:229], v162 offset:18432
	s_waitcnt vmcnt(8)
	s_waitcnt lgkmcnt(0)
	s_barrier
	s_waitcnt lgkmcnt(0)
	v_mfma_f32_16x16x128_f8f6f4 v[18:21], v[166:169], v[182:185], v[18:21] cbsz:4 blgp:4
	v_mfma_f32_16x16x128_f8f6f4 v[18:21], v[174:177], v[190:193], v[18:21] cbsz:4 blgp:4
	v_mfma_f32_16x16x128_f8f6f4 v[22:25], v[170:173], v[182:185], v[22:25] cbsz:4 blgp:4
	v_mfma_f32_16x16x128_f8f6f4 v[22:25], v[178:181], v[190:193], v[22:25] cbsz:4 blgp:4
	v_mfma_f32_16x16x128_f8f6f4 v[26:29], v[166:169], v[186:189], v[26:29] cbsz:4 blgp:4
	v_mfma_f32_16x16x128_f8f6f4 v[26:29], v[174:177], v[194:197], v[26:29] cbsz:4 blgp:4
	v_mfma_f32_16x16x128_f8f6f4 v[30:33], v[170:173], v[186:189], v[30:33] cbsz:4 blgp:4
	v_mfma_f32_16x16x128_f8f6f4 v[30:33], v[178:181], v[194:197], v[30:33] cbsz:4 blgp:4
	v_mfma_f32_16x16x128_f8f6f4 v[34:37], v[166:169], v[198:201], v[34:37] cbsz:4 blgp:4
	v_mfma_f32_16x16x128_f8f6f4 v[34:37], v[174:177], v[206:209], v[34:37] cbsz:4 blgp:4
	v_mfma_f32_16x16x128_f8f6f4 v[38:41], v[170:173], v[198:201], v[38:41] cbsz:4 blgp:4
	v_mfma_f32_16x16x128_f8f6f4 v[38:41], v[178:181], v[206:209], v[38:41] cbsz:4 blgp:4
	v_mfma_f32_16x16x128_f8f6f4 v[42:45], v[166:169], v[202:205], v[42:45] cbsz:4 blgp:4
	v_mfma_f32_16x16x128_f8f6f4 v[42:45], v[174:177], v[210:213], v[42:45] cbsz:4 blgp:4
	v_mfma_f32_16x16x128_f8f6f4 v[46:49], v[170:173], v[202:205], v[46:49] cbsz:4 blgp:4
	v_mfma_f32_16x16x128_f8f6f4 v[46:49], v[178:181], v[210:213], v[46:49] cbsz:4 blgp:4
	v_mfma_f32_16x16x128_f8f6f4 v[50:53], v[214:217], v[182:185], v[50:53] cbsz:4 blgp:4
	v_mfma_f32_16x16x128_f8f6f4 v[50:53], v[222:225], v[190:193], v[50:53] cbsz:4 blgp:4
	v_mfma_f32_16x16x128_f8f6f4 v[54:57], v[218:221], v[182:185], v[54:57] cbsz:4 blgp:4
	v_mfma_f32_16x16x128_f8f6f4 v[54:57], v[226:229], v[190:193], v[54:57] cbsz:4 blgp:4
	v_mfma_f32_16x16x128_f8f6f4 v[58:61], v[214:217], v[186:189], v[58:61] cbsz:4 blgp:4
	v_mfma_f32_16x16x128_f8f6f4 v[58:61], v[222:225], v[194:197], v[58:61] cbsz:4 blgp:4
	v_mfma_f32_16x16x128_f8f6f4 v[62:65], v[218:221], v[186:189], v[62:65] cbsz:4 blgp:4
	v_mfma_f32_16x16x128_f8f6f4 v[62:65], v[226:229], v[194:197], v[62:65] cbsz:4 blgp:4
	v_mfma_f32_16x16x128_f8f6f4 v[66:69], v[214:217], v[198:201], v[66:69] cbsz:4 blgp:4
	v_mfma_f32_16x16x128_f8f6f4 v[66:69], v[222:225], v[206:209], v[66:69] cbsz:4 blgp:4
	v_mfma_f32_16x16x128_f8f6f4 v[70:73], v[218:221], v[198:201], v[70:73] cbsz:4 blgp:4
	v_mfma_f32_16x16x128_f8f6f4 v[70:73], v[226:229], v[206:209], v[70:73] cbsz:4 blgp:4
	v_mfma_f32_16x16x128_f8f6f4 v[74:77], v[214:217], v[202:205], v[74:77] cbsz:4 blgp:4
	v_mfma_f32_16x16x128_f8f6f4 v[74:77], v[222:225], v[210:213], v[74:77] cbsz:4 blgp:4
	v_mfma_f32_16x16x128_f8f6f4 v[78:81], v[218:221], v[202:205], v[78:81] cbsz:4 blgp:4
	v_mfma_f32_16x16x128_f8f6f4 v[78:81], v[226:229], v[210:213], v[78:81] cbsz:4 blgp:4
	s_barrier
	s_mov_b32 m0, s55
	s_nop 0
	global_load_lds_dwordx4 v148, s[48:49]
	s_mov_b32 m0, s56
	s_nop 0
	global_load_lds_dwordx4 v152, s[48:49]
	ds_read_b128 v[182:185], v163 offset:16384
	ds_read_b128 v[186:189], v163 offset:18432
	ds_read_b128 v[190:193], v164 offset:16384
	ds_read_b128 v[194:197], v164 offset:18432
	ds_read_b128 v[198:201], v163 offset:20480
	ds_read_b128 v[202:205], v163 offset:22528
	ds_read_b128 v[206:209], v164 offset:20480
	ds_read_b128 v[210:213], v164 offset:22528
	s_mov_b32 m0, s54
	s_nop 0
	global_load_lds_dwordx4 v146, s[46:47]
	s_mov_b32 m0, s57
	s_nop 0
	global_load_lds_dwordx4 v150, s[46:47]
	s_add_u32 s48, s48, s24
	s_addc_u32 s49, s49, s25
	s_mov_b32 m0, s58
	s_nop 0
	global_load_lds_dwordx4 v148, s[48:49]
	s_mov_b32 m0, s59
	s_nop 0
	global_load_lds_dwordx4 v152, s[48:49]
	s_waitcnt vmcnt(8)
	s_waitcnt lgkmcnt(0)
	s_barrier
	v_mfma_f32_16x16x128_f8f6f4 v[86:89], v[166:169], v[182:185], v[86:89] cbsz:4 blgp:4
	v_mfma_f32_16x16x128_f8f6f4 v[86:89], v[174:177], v[190:193], v[86:89] cbsz:4 blgp:4
	v_mfma_f32_16x16x128_f8f6f4 v[90:93], v[170:173], v[182:185], v[90:93] cbsz:4 blgp:4
	v_mfma_f32_16x16x128_f8f6f4 v[90:93], v[178:181], v[190:193], v[90:93] cbsz:4 blgp:4
	v_mfma_f32_16x16x128_f8f6f4 v[98:101], v[166:169], v[186:189], v[98:101] cbsz:4 blgp:4
	v_mfma_f32_16x16x128_f8f6f4 v[98:101], v[174:177], v[194:197], v[98:101] cbsz:4 blgp:4
	v_mfma_f32_16x16x128_f8f6f4 v[106:109], v[170:173], v[186:189], v[106:109] cbsz:4 blgp:4
	v_mfma_f32_16x16x128_f8f6f4 v[106:109], v[178:181], v[194:197], v[106:109] cbsz:4 blgp:4
	v_mfma_f32_16x16x128_f8f6f4 v[118:121], v[166:169], v[198:201], v[118:121] cbsz:4 blgp:4
	v_mfma_f32_16x16x128_f8f6f4 v[118:121], v[174:177], v[206:209], v[118:121] cbsz:4 blgp:4
	v_mfma_f32_16x16x128_f8f6f4 v[126:129], v[170:173], v[198:201], v[126:129] cbsz:4 blgp:4
	v_mfma_f32_16x16x128_f8f6f4 v[126:129], v[178:181], v[206:209], v[126:129] cbsz:4 blgp:4
	v_mfma_f32_16x16x128_f8f6f4 v[138:141], v[166:169], v[202:205], v[138:141] cbsz:4 blgp:4
	v_mfma_f32_16x16x128_f8f6f4 v[138:141], v[174:177], v[210:213], v[138:141] cbsz:4 blgp:4
	v_mfma_f32_16x16x128_f8f6f4 v[82:85], v[170:173], v[202:205], v[82:85] cbsz:4 blgp:4
	v_mfma_f32_16x16x128_f8f6f4 v[82:85], v[178:181], v[210:213], v[82:85] cbsz:4 blgp:4
	v_mfma_f32_16x16x128_f8f6f4 v[94:97], v[214:217], v[182:185], v[94:97] cbsz:4 blgp:4
	v_mfma_f32_16x16x128_f8f6f4 v[94:97], v[222:225], v[190:193], v[94:97] cbsz:4 blgp:4
	v_mfma_f32_16x16x128_f8f6f4 v[102:105], v[218:221], v[182:185], v[102:105] cbsz:4 blgp:4
	v_mfma_f32_16x16x128_f8f6f4 v[102:105], v[226:229], v[190:193], v[102:105] cbsz:4 blgp:4
	v_mfma_f32_16x16x128_f8f6f4 v[110:113], v[214:217], v[186:189], v[110:113] cbsz:4 blgp:4
	v_mfma_f32_16x16x128_f8f6f4 v[110:113], v[222:225], v[194:197], v[110:113] cbsz:4 blgp:4
	v_mfma_f32_16x16x128_f8f6f4 v[114:117], v[218:221], v[186:189], v[114:117] cbsz:4 blgp:4
	v_mfma_f32_16x16x128_f8f6f4 v[114:117], v[226:229], v[194:197], v[114:117] cbsz:4 blgp:4
	v_mfma_f32_16x16x128_f8f6f4 v[122:125], v[214:217], v[198:201], v[122:125] cbsz:4 blgp:4
	v_mfma_f32_16x16x128_f8f6f4 v[122:125], v[222:225], v[206:209], v[122:125] cbsz:4 blgp:4
	v_mfma_f32_16x16x128_f8f6f4 v[130:133], v[218:221], v[198:201], v[130:133] cbsz:4 blgp:4
	v_mfma_f32_16x16x128_f8f6f4 v[130:133], v[226:229], v[206:209], v[130:133] cbsz:4 blgp:4
	v_mfma_f32_16x16x128_f8f6f4 v[134:137], v[214:217], v[202:205], v[134:137] cbsz:4 blgp:4
	v_mfma_f32_16x16x128_f8f6f4 v[134:137], v[222:225], v[210:213], v[134:137] cbsz:4 blgp:4
	v_mfma_f32_16x16x128_f8f6f4 v[142:145], v[218:221], v[202:205], v[142:145] cbsz:4 blgp:4
	v_mfma_f32_16x16x128_f8f6f4 v[142:145], v[226:229], v[210:213], v[142:145] cbsz:4 blgp:4
	s_barrier
	ds_read_b128 v[166:169], v161 offset:32768
	ds_read_b128 v[170:173], v161 offset:34816
	ds_read_b128 v[174:177], v162 offset:32768
	ds_read_b128 v[178:181], v162 offset:34816
	ds_read_b128 v[182:185], v163 offset:32768
	ds_read_b128 v[186:189], v163 offset:34816
	ds_read_b128 v[190:193], v164 offset:32768
	ds_read_b128 v[194:197], v164 offset:34816
	ds_read_b128 v[198:201], v163 offset:36864
	ds_read_b128 v[202:205], v163 offset:38912
	ds_read_b128 v[206:209], v164 offset:36864
	ds_read_b128 v[210:213], v164 offset:38912
	s_add_u32 s46, s46, s22
	s_addc_u32 s47, s47, s23
	s_mov_b32 m0, s60
	s_nop 0
	global_load_lds_dwordx4 v146, s[46:47]
	s_mov_b32 m0, s61
	s_nop 0
	global_load_lds_dwordx4 v150, s[46:47]
	s_waitcnt lgkmcnt(8)
	ds_read_b128 v[214:217], v161 offset:49152
	ds_read_b128 v[218:221], v161 offset:51200
	ds_read_b128 v[222:225], v162 offset:49152
	ds_read_b128 v[226:229], v162 offset:51200
	s_waitcnt vmcnt(8)
	s_waitcnt lgkmcnt(0)
	s_barrier
	s_waitcnt lgkmcnt(0)
	v_mfma_f32_16x16x128_f8f6f4 v[18:21], v[166:169], v[182:185], v[18:21] cbsz:4 blgp:4
	v_mfma_f32_16x16x128_f8f6f4 v[18:21], v[174:177], v[190:193], v[18:21] cbsz:4 blgp:4
	v_mfma_f32_16x16x128_f8f6f4 v[22:25], v[170:173], v[182:185], v[22:25] cbsz:4 blgp:4
	v_mfma_f32_16x16x128_f8f6f4 v[22:25], v[178:181], v[190:193], v[22:25] cbsz:4 blgp:4
	v_mfma_f32_16x16x128_f8f6f4 v[26:29], v[166:169], v[186:189], v[26:29] cbsz:4 blgp:4
	v_mfma_f32_16x16x128_f8f6f4 v[26:29], v[174:177], v[194:197], v[26:29] cbsz:4 blgp:4
	v_mfma_f32_16x16x128_f8f6f4 v[30:33], v[170:173], v[186:189], v[30:33] cbsz:4 blgp:4
	v_mfma_f32_16x16x128_f8f6f4 v[30:33], v[178:181], v[194:197], v[30:33] cbsz:4 blgp:4
	v_mfma_f32_16x16x128_f8f6f4 v[34:37], v[166:169], v[198:201], v[34:37] cbsz:4 blgp:4
	v_mfma_f32_16x16x128_f8f6f4 v[34:37], v[174:177], v[206:209], v[34:37] cbsz:4 blgp:4
	v_mfma_f32_16x16x128_f8f6f4 v[38:41], v[170:173], v[198:201], v[38:41] cbsz:4 blgp:4
	v_mfma_f32_16x16x128_f8f6f4 v[38:41], v[178:181], v[206:209], v[38:41] cbsz:4 blgp:4
	v_mfma_f32_16x16x128_f8f6f4 v[42:45], v[166:169], v[202:205], v[42:45] cbsz:4 blgp:4
	v_mfma_f32_16x16x128_f8f6f4 v[42:45], v[174:177], v[210:213], v[42:45] cbsz:4 blgp:4
	v_mfma_f32_16x16x128_f8f6f4 v[46:49], v[170:173], v[202:205], v[46:49] cbsz:4 blgp:4
	v_mfma_f32_16x16x128_f8f6f4 v[46:49], v[178:181], v[210:213], v[46:49] cbsz:4 blgp:4
	v_mfma_f32_16x16x128_f8f6f4 v[50:53], v[214:217], v[182:185], v[50:53] cbsz:4 blgp:4
	v_mfma_f32_16x16x128_f8f6f4 v[50:53], v[222:225], v[190:193], v[50:53] cbsz:4 blgp:4
	v_mfma_f32_16x16x128_f8f6f4 v[54:57], v[218:221], v[182:185], v[54:57] cbsz:4 blgp:4
	v_mfma_f32_16x16x128_f8f6f4 v[54:57], v[226:229], v[190:193], v[54:57] cbsz:4 blgp:4
	v_mfma_f32_16x16x128_f8f6f4 v[58:61], v[214:217], v[186:189], v[58:61] cbsz:4 blgp:4
	v_mfma_f32_16x16x128_f8f6f4 v[58:61], v[222:225], v[194:197], v[58:61] cbsz:4 blgp:4
	v_mfma_f32_16x16x128_f8f6f4 v[62:65], v[218:221], v[186:189], v[62:65] cbsz:4 blgp:4
	v_mfma_f32_16x16x128_f8f6f4 v[62:65], v[226:229], v[194:197], v[62:65] cbsz:4 blgp:4
	v_mfma_f32_16x16x128_f8f6f4 v[66:69], v[214:217], v[198:201], v[66:69] cbsz:4 blgp:4
	v_mfma_f32_16x16x128_f8f6f4 v[66:69], v[222:225], v[206:209], v[66:69] cbsz:4 blgp:4
	v_mfma_f32_16x16x128_f8f6f4 v[70:73], v[218:221], v[198:201], v[70:73] cbsz:4 blgp:4
	v_mfma_f32_16x16x128_f8f6f4 v[70:73], v[226:229], v[206:209], v[70:73] cbsz:4 blgp:4
	v_mfma_f32_16x16x128_f8f6f4 v[74:77], v[214:217], v[202:205], v[74:77] cbsz:4 blgp:4
	v_mfma_f32_16x16x128_f8f6f4 v[74:77], v[222:225], v[210:213], v[74:77] cbsz:4 blgp:4
	v_mfma_f32_16x16x128_f8f6f4 v[78:81], v[218:221], v[202:205], v[78:81] cbsz:4 blgp:4
	v_mfma_f32_16x16x128_f8f6f4 v[78:81], v[226:229], v[210:213], v[78:81] cbsz:4 blgp:4
	s_barrier
	s_mov_b32 m0, s64
	s_nop 0
	global_load_lds_dwordx4 v148, s[40:41]
	s_mov_b32 m0, s65
	s_nop 0
	global_load_lds_dwordx4 v152, s[40:41]
	ds_read_b128 v[182:185], v163 offset:49152
	ds_read_b128 v[186:189], v163 offset:51200
	ds_read_b128 v[190:193], v164 offset:49152
	ds_read_b128 v[194:197], v164 offset:51200
	ds_read_b128 v[198:201], v163 offset:53248
	ds_read_b128 v[202:205], v163 offset:55296
	ds_read_b128 v[206:209], v164 offset:53248
	ds_read_b128 v[210:213], v164 offset:55296
	s_mov_b32 m0, s66
	s_nop 0
	global_load_lds_dwordx4 v146, s[44:45]
	s_mov_b32 m0, s67
	s_nop 0
	global_load_lds_dwordx4 v150, s[44:45]
	s_add_u32 s40, s40, s24
	s_addc_u32 s41, s41, s25
	s_mov_b32 m0, s68
	s_nop 0
	global_load_lds_dwordx4 v148, s[40:41]
	s_mov_b32 m0, s69
	s_nop 0
	global_load_lds_dwordx4 v152, s[40:41]
	s_waitcnt vmcnt(8)
	s_waitcnt lgkmcnt(0)
	s_barrier
	v_mfma_f32_16x16x128_f8f6f4 v[86:89], v[166:169], v[182:185], v[86:89] cbsz:4 blgp:4
	v_mfma_f32_16x16x128_f8f6f4 v[86:89], v[174:177], v[190:193], v[86:89] cbsz:4 blgp:4
	v_mfma_f32_16x16x128_f8f6f4 v[90:93], v[170:173], v[182:185], v[90:93] cbsz:4 blgp:4
	v_mfma_f32_16x16x128_f8f6f4 v[90:93], v[178:181], v[190:193], v[90:93] cbsz:4 blgp:4
	v_mfma_f32_16x16x128_f8f6f4 v[98:101], v[166:169], v[186:189], v[98:101] cbsz:4 blgp:4
	v_mfma_f32_16x16x128_f8f6f4 v[98:101], v[174:177], v[194:197], v[98:101] cbsz:4 blgp:4
	v_mfma_f32_16x16x128_f8f6f4 v[106:109], v[170:173], v[186:189], v[106:109] cbsz:4 blgp:4
	v_mfma_f32_16x16x128_f8f6f4 v[106:109], v[178:181], v[194:197], v[106:109] cbsz:4 blgp:4
	v_mfma_f32_16x16x128_f8f6f4 v[118:121], v[166:169], v[198:201], v[118:121] cbsz:4 blgp:4
	v_mfma_f32_16x16x128_f8f6f4 v[118:121], v[174:177], v[206:209], v[118:121] cbsz:4 blgp:4
	v_mfma_f32_16x16x128_f8f6f4 v[126:129], v[170:173], v[198:201], v[126:129] cbsz:4 blgp:4
	v_mfma_f32_16x16x128_f8f6f4 v[126:129], v[178:181], v[206:209], v[126:129] cbsz:4 blgp:4
	v_mfma_f32_16x16x128_f8f6f4 v[138:141], v[166:169], v[202:205], v[138:141] cbsz:4 blgp:4
	v_mfma_f32_16x16x128_f8f6f4 v[138:141], v[174:177], v[210:213], v[138:141] cbsz:4 blgp:4
	v_mfma_f32_16x16x128_f8f6f4 v[82:85], v[170:173], v[202:205], v[82:85] cbsz:4 blgp:4
	v_mfma_f32_16x16x128_f8f6f4 v[82:85], v[178:181], v[210:213], v[82:85] cbsz:4 blgp:4
	v_mfma_f32_16x16x128_f8f6f4 v[94:97], v[214:217], v[182:185], v[94:97] cbsz:4 blgp:4
	v_mfma_f32_16x16x128_f8f6f4 v[94:97], v[222:225], v[190:193], v[94:97] cbsz:4 blgp:4
	v_mfma_f32_16x16x128_f8f6f4 v[102:105], v[218:221], v[182:185], v[102:105] cbsz:4 blgp:4
	v_mfma_f32_16x16x128_f8f6f4 v[102:105], v[226:229], v[190:193], v[102:105] cbsz:4 blgp:4
	v_mfma_f32_16x16x128_f8f6f4 v[110:113], v[214:217], v[186:189], v[110:113] cbsz:4 blgp:4
	v_mfma_f32_16x16x128_f8f6f4 v[110:113], v[222:225], v[194:197], v[110:113] cbsz:4 blgp:4
	v_mfma_f32_16x16x128_f8f6f4 v[114:117], v[218:221], v[186:189], v[114:117] cbsz:4 blgp:4
	v_mfma_f32_16x16x128_f8f6f4 v[114:117], v[226:229], v[194:197], v[114:117] cbsz:4 blgp:4
	v_mfma_f32_16x16x128_f8f6f4 v[122:125], v[214:217], v[198:201], v[122:125] cbsz:4 blgp:4
	v_mfma_f32_16x16x128_f8f6f4 v[122:125], v[222:225], v[206:209], v[122:125] cbsz:4 blgp:4
	v_mfma_f32_16x16x128_f8f6f4 v[130:133], v[218:221], v[198:201], v[130:133] cbsz:4 blgp:4
	v_mfma_f32_16x16x128_f8f6f4 v[130:133], v[226:229], v[206:209], v[130:133] cbsz:4 blgp:4
	v_mfma_f32_16x16x128_f8f6f4 v[134:137], v[214:217], v[202:205], v[134:137] cbsz:4 blgp:4
	v_mfma_f32_16x16x128_f8f6f4 v[134:137], v[222:225], v[210:213], v[134:137] cbsz:4 blgp:4
	v_mfma_f32_16x16x128_f8f6f4 v[142:145], v[218:221], v[202:205], v[142:145] cbsz:4 blgp:4
	v_mfma_f32_16x16x128_f8f6f4 v[142:145], v[226:229], v[210:213], v[142:145] cbsz:4 blgp:4
	s_add_i32 s40, s81, 2
	s_add_u32 s29, s29, 0x100
	s_addc_u32 s78, s78, 0
	s_add_u32 s79, s79, 0x100
	s_addc_u32 s80, s80, 0
	s_add_u32 s38, s38, 0x100
	s_addc_u32 s39, s39, 0
	s_cmp_ge_i32 s81, s63
	s_barrier
	s_cbranch_scc1 .LBB4_4
	s_mov_b32 s81, s40
	s_cmp_eq_u32 s63, s81
	s_cselect_b64 s[40:41], -1, 0
	s_cmp_lg_u32 s63, s81
	s_cbranch_scc0 .LBB4_14
	s_branch .LBB4_15

.Lrs_a_5:
	s_add_u32 s82, s42, s22
	s_addc_u32 s83, s43, s23
	s_add_u32 s29, s42, 0x100
	s_addc_u32 s46, s43, 0
	s_and_b64 s[44:45], s[14:15], exec
	ds_read_b128 v[82:85], v163
	ds_read_b128 v[94:97], v163 offset:2048
	ds_read_b128 v[102:105], v164
	ds_read_b128 v[110:113], v164 offset:2048
	s_cselect_b32 s49, s39, s46
	s_cselect_b32 s48, s38, s29
	s_add_u32 s29, s40, 0x100
	s_addc_u32 s46, s41, 0
	s_and_b64 s[44:45], s[14:15], exec
	s_cselect_b32 s51, s5, s46
	s_cselect_b32 s50, s4, s29
	s_add_u32 s46, s48, 0x80
	s_addc_u32 s47, s49, 0
	s_add_u32 s44, s50, 0x80
	s_addc_u32 s45, s51, 0
	ds_read_b128 v[58:61], v165
	ds_read_b128 v[66:69], v165 offset:2048
	ds_read_b128 v[62:65], v166
	ds_read_b128 v[70:73], v166 offset:2048
	ds_read_b128 v[74:77], v165 offset:4096
	ds_read_b128 v[86:89], v165 offset:6144
	ds_read_b128 v[78:81], v166 offset:4096
	ds_read_b128 v[90:93], v166 offset:6144
	s_add_u32 s80, s82, 0x80
	s_addc_u32 s81, s83, 0
	s_mov_b32 m0, s71
	s_nop 0
	global_load_lds_dwordx4 v146, s[80:81]
	s_mov_b32 m0, s72
	s_nop 0
	global_load_lds_dwordx4 v150, s[80:81]
	s_waitcnt lgkmcnt(8)
	ds_read_b128 v[142:145], v163 offset:16384
	ds_read_b128 v[156:159], v163 offset:18432
	ds_read_b128 v[168:171], v164 offset:16384
	ds_read_b128 v[172:175], v164 offset:18432
	s_waitcnt vmcnt(8)
	s_waitcnt lgkmcnt(0)
	s_barrier
	s_waitcnt lgkmcnt(0)
	s_waitcnt vmcnt(16)
	v_mov_b32_e32 v1, v0
	v_pk_mul_f32 v[16:17], v[0:1], v[16:17]
	v_pk_mul_f32 v[14:15], v[154:155], v[14:15]
	v_pk_mul_f32 v[12:13], v[0:1], v[12:13]
	v_pk_mul_f32 v[10:11], v[154:155], v[10:11]
	v_pk_mul_f32 v[8:9], v[0:1], v[8:9]
	v_pk_mul_f32 v[6:7], v[154:155], v[6:7]
	v_pk_mul_f32 v[4:5], v[0:1], v[4:5]
	v_pk_mul_f32 v[2:3], v[154:155], v[2:3]
	v_mfma_f32_16x16x128_f8f6f4 v[18:21], v[82:85], v[58:61], v[14:17] cbsz:4 blgp:4
	v_mfma_f32_16x16x128_f8f6f4 v[18:21], v[102:105], v[62:65], v[18:21] cbsz:4 blgp:4
	v_mfma_f32_16x16x128_f8f6f4 v[22:25], v[94:97], v[58:61], v[10:13] cbsz:4 blgp:4
	v_mfma_f32_16x16x128_f8f6f4 v[22:25], v[110:113], v[62:65], v[22:25] cbsz:4 blgp:4
	v_mfma_f32_16x16x128_f8f6f4 v[26:29], v[82:85], v[66:69], v[14:17] cbsz:4 blgp:4
	v_mfma_f32_16x16x128_f8f6f4 v[26:29], v[102:105], v[70:73], v[26:29] cbsz:4 blgp:4
	v_mfma_f32_16x16x128_f8f6f4 v[30:33], v[94:97], v[66:69], v[10:13] cbsz:4 blgp:4
	v_mfma_f32_16x16x128_f8f6f4 v[30:33], v[110:113], v[70:73], v[30:33] cbsz:4 blgp:4
	v_mfma_f32_16x16x128_f8f6f4 v[34:37], v[82:85], v[74:77], v[14:17] cbsz:4 blgp:4
	v_mfma_f32_16x16x128_f8f6f4 v[34:37], v[102:105], v[78:81], v[34:37] cbsz:4 blgp:4
	v_mfma_f32_16x16x128_f8f6f4 v[38:41], v[94:97], v[74:77], v[10:13] cbsz:4 blgp:4
	v_mfma_f32_16x16x128_f8f6f4 v[38:41], v[110:113], v[78:81], v[38:41] cbsz:4 blgp:4
	v_mfma_f32_16x16x128_f8f6f4 v[42:45], v[82:85], v[86:89], v[14:17] cbsz:4 blgp:4
	v_mfma_f32_16x16x128_f8f6f4 v[42:45], v[102:105], v[90:93], v[42:45] cbsz:4 blgp:4
	v_mfma_f32_16x16x128_f8f6f4 v[46:49], v[94:97], v[86:89], v[10:13] cbsz:4 blgp:4
	v_mfma_f32_16x16x128_f8f6f4 v[46:49], v[110:113], v[90:93], v[46:49] cbsz:4 blgp:4
	v_mfma_f32_16x16x128_f8f6f4 v[50:53], v[142:145], v[58:61], v[6:9] cbsz:4 blgp:4
	v_mfma_f32_16x16x128_f8f6f4 v[50:53], v[168:171], v[62:65], v[50:53] cbsz:4 blgp:4
	v_mfma_f32_16x16x128_f8f6f4 v[54:57], v[156:159], v[58:61], v[2:5] cbsz:4 blgp:4
	v_mfma_f32_16x16x128_f8f6f4 v[54:57], v[172:175], v[62:65], v[54:57] cbsz:4 blgp:4
	v_mfma_f32_16x16x128_f8f6f4 v[58:61], v[142:145], v[66:69], v[6:9] cbsz:4 blgp:4
	v_mfma_f32_16x16x128_f8f6f4 v[58:61], v[168:171], v[70:73], v[58:61] cbsz:4 blgp:4
	v_mfma_f32_16x16x128_f8f6f4 v[62:65], v[156:159], v[66:69], v[2:5] cbsz:4 blgp:4
	v_mfma_f32_16x16x128_f8f6f4 v[62:65], v[172:175], v[70:73], v[62:65] cbsz:4 blgp:4
	v_mfma_f32_16x16x128_f8f6f4 v[66:69], v[142:145], v[74:77], v[6:9] cbsz:4 blgp:4
	v_mfma_f32_16x16x128_f8f6f4 v[66:69], v[168:171], v[78:81], v[66:69] cbsz:4 blgp:4
	v_mfma_f32_16x16x128_f8f6f4 v[70:73], v[156:159], v[74:77], v[2:5] cbsz:4 blgp:4
	v_mfma_f32_16x16x128_f8f6f4 v[70:73], v[172:175], v[78:81], v[70:73] cbsz:4 blgp:4
	v_mfma_f32_16x16x128_f8f6f4 v[74:77], v[142:145], v[86:89], v[6:9] cbsz:4 blgp:4
	v_mfma_f32_16x16x128_f8f6f4 v[74:77], v[168:171], v[90:93], v[74:77] cbsz:4 blgp:4
	v_mfma_f32_16x16x128_f8f6f4 v[78:81], v[156:159], v[86:89], v[2:5] cbsz:4 blgp:4
	v_mfma_f32_16x16x128_f8f6f4 v[78:81], v[172:175], v[90:93], v[78:81] cbsz:4 blgp:4
	s_barrier
	s_mov_b32 m0, s56
	s_nop 0
	global_load_lds_dwordx4 v148, s[50:51]
	s_mov_b32 m0, s57
	s_nop 0
	global_load_lds_dwordx4 v152, s[50:51]
	ds_read_b128 v[114:117], v165 offset:16384
	ds_read_b128 v[122:125], v165 offset:18432
	ds_read_b128 v[130:133], v166 offset:16384
	ds_read_b128 v[134:137], v166 offset:18432
	ds_read_b128 v[176:179], v165 offset:20480
	ds_read_b128 v[180:183], v165 offset:22528
	ds_read_b128 v[184:187], v166 offset:20480
	ds_read_b128 v[188:191], v166 offset:22528
	s_mov_b32 m0, s55
	s_nop 0
	global_load_lds_dwordx4 v146, s[48:49]
	s_mov_b32 m0, s58
	s_nop 0
	global_load_lds_dwordx4 v150, s[48:49]
	s_add_u32 s50, s50, s24
	s_addc_u32 s51, s51, s25
	s_mov_b32 m0, s59
	s_nop 0
	global_load_lds_dwordx4 v148, s[50:51]
	s_mov_b32 m0, s60
	s_nop 0
	global_load_lds_dwordx4 v152, s[50:51]
	s_waitcnt vmcnt(8)
	s_waitcnt lgkmcnt(0)
	s_barrier
	v_mfma_f32_16x16x128_f8f6f4 v[86:89], v[82:85], v[114:117], v[14:17] cbsz:4 blgp:4
	v_mfma_f32_16x16x128_f8f6f4 v[86:89], v[102:105], v[130:133], v[86:89] cbsz:4 blgp:4
	v_mfma_f32_16x16x128_f8f6f4 v[90:93], v[94:97], v[114:117], v[10:13] cbsz:4 blgp:4
	v_mfma_f32_16x16x128_f8f6f4 v[90:93], v[110:113], v[130:133], v[90:93] cbsz:4 blgp:4
	v_mfma_f32_16x16x128_f8f6f4 v[98:101], v[82:85], v[122:125], v[14:17] cbsz:4 blgp:4
	v_mfma_f32_16x16x128_f8f6f4 v[98:101], v[102:105], v[134:137], v[98:101] cbsz:4 blgp:4
	v_mfma_f32_16x16x128_f8f6f4 v[106:109], v[94:97], v[122:125], v[10:13] cbsz:4 blgp:4
	v_mfma_f32_16x16x128_f8f6f4 v[106:109], v[110:113], v[134:137], v[106:109] cbsz:4 blgp:4
	v_mfma_f32_16x16x128_f8f6f4 v[118:121], v[82:85], v[176:179], v[14:17] cbsz:4 blgp:4
	v_mfma_f32_16x16x128_f8f6f4 v[118:121], v[102:105], v[184:187], v[118:121] cbsz:4 blgp:4
	v_mfma_f32_16x16x128_f8f6f4 v[126:129], v[94:97], v[176:179], v[10:13] cbsz:4 blgp:4
	v_mfma_f32_16x16x128_f8f6f4 v[126:129], v[110:113], v[184:187], v[126:129] cbsz:4 blgp:4
	v_mfma_f32_16x16x128_f8f6f4 v[138:141], v[82:85], v[180:183], v[14:17] cbsz:4 blgp:4
	v_mfma_f32_16x16x128_f8f6f4 v[138:141], v[102:105], v[188:191], v[138:141] cbsz:4 blgp:4
	v_mfma_f32_16x16x128_f8f6f4 v[82:85], v[94:97], v[180:183], v[10:13] cbsz:4 blgp:4
	v_mfma_f32_16x16x128_f8f6f4 v[82:85], v[110:113], v[188:191], v[82:85] cbsz:4 blgp:4
	v_mfma_f32_16x16x128_f8f6f4 v[94:97], v[142:145], v[114:117], v[6:9] cbsz:4 blgp:4
	v_mfma_f32_16x16x128_f8f6f4 v[94:97], v[168:171], v[130:133], v[94:97] cbsz:4 blgp:4
	v_mfma_f32_16x16x128_f8f6f4 v[102:105], v[156:159], v[114:117], v[2:5] cbsz:4 blgp:4
	v_mfma_f32_16x16x128_f8f6f4 v[102:105], v[172:175], v[130:133], v[102:105] cbsz:4 blgp:4
	v_mfma_f32_16x16x128_f8f6f4 v[110:113], v[142:145], v[122:125], v[6:9] cbsz:4 blgp:4
	v_mfma_f32_16x16x128_f8f6f4 v[110:113], v[168:171], v[134:137], v[110:113] cbsz:4 blgp:4
	v_mfma_f32_16x16x128_f8f6f4 v[114:117], v[156:159], v[122:125], v[2:5] cbsz:4 blgp:4
	v_mfma_f32_16x16x128_f8f6f4 v[114:117], v[172:175], v[134:137], v[114:117] cbsz:4 blgp:4
	v_mfma_f32_16x16x128_f8f6f4 v[122:125], v[142:145], v[176:179], v[6:9] cbsz:4 blgp:4
	v_mfma_f32_16x16x128_f8f6f4 v[122:125], v[168:171], v[184:187], v[122:125] cbsz:4 blgp:4
	v_mfma_f32_16x16x128_f8f6f4 v[130:133], v[156:159], v[176:179], v[2:5] cbsz:4 blgp:4
	v_mfma_f32_16x16x128_f8f6f4 v[130:133], v[172:175], v[184:187], v[130:133] cbsz:4 blgp:4
	v_mfma_f32_16x16x128_f8f6f4 v[134:137], v[142:145], v[180:183], v[6:9] cbsz:4 blgp:4
	v_mfma_f32_16x16x128_f8f6f4 v[134:137], v[168:171], v[188:191], v[134:137] cbsz:4 blgp:4
	v_mfma_f32_16x16x128_f8f6f4 v[142:145], v[156:159], v[180:183], v[2:5] cbsz:4 blgp:4
	v_mfma_f32_16x16x128_f8f6f4 v[142:145], v[172:175], v[188:191], v[142:145] cbsz:4 blgp:4
	s_barrier
	ds_read_b128 v[156:159], v163 offset:32768
	ds_read_b128 v[168:171], v163 offset:34816
	ds_read_b128 v[172:175], v164 offset:32768
	ds_read_b128 v[176:179], v164 offset:34816
	ds_read_b128 v[180:183], v165 offset:32768
	ds_read_b128 v[184:187], v165 offset:34816
	ds_read_b128 v[188:191], v166 offset:32768
	ds_read_b128 v[192:195], v166 offset:34816
	ds_read_b128 v[196:199], v165 offset:36864
	ds_read_b128 v[200:203], v165 offset:38912
	ds_read_b128 v[204:207], v166 offset:36864
	ds_read_b128 v[208:211], v166 offset:38912
	s_add_u32 s48, s48, s22
	s_addc_u32 s49, s49, s23
	s_mov_b32 m0, s61
	s_nop 0
	global_load_lds_dwordx4 v146, s[48:49]
	s_mov_b32 m0, s62
	s_nop 0
	global_load_lds_dwordx4 v150, s[48:49]
	s_waitcnt lgkmcnt(8)
	ds_read_b128 v[212:215], v163 offset:49152
	ds_read_b128 v[216:219], v163 offset:51200
	ds_read_b128 v[220:223], v164 offset:49152
	ds_read_b128 v[224:227], v164 offset:51200
	s_waitcnt vmcnt(8)
	s_waitcnt lgkmcnt(0)
	s_barrier
	s_waitcnt lgkmcnt(0)
	v_mfma_f32_16x16x128_f8f6f4 v[18:21], v[156:159], v[180:183], v[18:21] cbsz:4 blgp:4
	v_mfma_f32_16x16x128_f8f6f4 v[18:21], v[172:175], v[188:191], v[18:21] cbsz:4 blgp:4
	v_mfma_f32_16x16x128_f8f6f4 v[22:25], v[168:171], v[180:183], v[22:25] cbsz:4 blgp:4
	v_mfma_f32_16x16x128_f8f6f4 v[22:25], v[176:179], v[188:191], v[22:25] cbsz:4 blgp:4
	v_mfma_f32_16x16x128_f8f6f4 v[26:29], v[156:159], v[184:187], v[26:29] cbsz:4 blgp:4
	v_mfma_f32_16x16x128_f8f6f4 v[26:29], v[172:175], v[192:195], v[26:29] cbsz:4 blgp:4
	v_mfma_f32_16x16x128_f8f6f4 v[30:33], v[168:171], v[184:187], v[30:33] cbsz:4 blgp:4
	v_mfma_f32_16x16x128_f8f6f4 v[30:33], v[176:179], v[192:195], v[30:33] cbsz:4 blgp:4
	v_mfma_f32_16x16x128_f8f6f4 v[34:37], v[156:159], v[196:199], v[34:37] cbsz:4 blgp:4
	v_mfma_f32_16x16x128_f8f6f4 v[34:37], v[172:175], v[204:207], v[34:37] cbsz:4 blgp:4
	v_mfma_f32_16x16x128_f8f6f4 v[38:41], v[168:171], v[196:199], v[38:41] cbsz:4 blgp:4
	v_mfma_f32_16x16x128_f8f6f4 v[38:41], v[176:179], v[204:207], v[38:41] cbsz:4 blgp:4
	v_mfma_f32_16x16x128_f8f6f4 v[42:45], v[156:159], v[200:203], v[42:45] cbsz:4 blgp:4
	v_mfma_f32_16x16x128_f8f6f4 v[42:45], v[172:175], v[208:211], v[42:45] cbsz:4 blgp:4
	v_mfma_f32_16x16x128_f8f6f4 v[46:49], v[168:171], v[200:203], v[46:49] cbsz:4 blgp:4
	v_mfma_f32_16x16x128_f8f6f4 v[46:49], v[176:179], v[208:211], v[46:49] cbsz:4 blgp:4
	v_mfma_f32_16x16x128_f8f6f4 v[50:53], v[212:215], v[180:183], v[50:53] cbsz:4 blgp:4
	v_mfma_f32_16x16x128_f8f6f4 v[50:53], v[220:223], v[188:191], v[50:53] cbsz:4 blgp:4
	v_mfma_f32_16x16x128_f8f6f4 v[54:57], v[216:219], v[180:183], v[54:57] cbsz:4 blgp:4
	v_mfma_f32_16x16x128_f8f6f4 v[54:57], v[224:227], v[188:191], v[54:57] cbsz:4 blgp:4
	v_mfma_f32_16x16x128_f8f6f4 v[58:61], v[212:215], v[184:187], v[58:61] cbsz:4 blgp:4
	v_mfma_f32_16x16x128_f8f6f4 v[58:61], v[220:223], v[192:195], v[58:61] cbsz:4 blgp:4
	v_mfma_f32_16x16x128_f8f6f4 v[62:65], v[216:219], v[184:187], v[62:65] cbsz:4 blgp:4
	v_mfma_f32_16x16x128_f8f6f4 v[62:65], v[224:227], v[192:195], v[62:65] cbsz:4 blgp:4
	v_mfma_f32_16x16x128_f8f6f4 v[66:69], v[212:215], v[196:199], v[66:69] cbsz:4 blgp:4
	v_mfma_f32_16x16x128_f8f6f4 v[66:69], v[220:223], v[204:207], v[66:69] cbsz:4 blgp:4
	v_mfma_f32_16x16x128_f8f6f4 v[70:73], v[216:219], v[196:199], v[70:73] cbsz:4 blgp:4
	v_mfma_f32_16x16x128_f8f6f4 v[70:73], v[224:227], v[204:207], v[70:73] cbsz:4 blgp:4
	v_mfma_f32_16x16x128_f8f6f4 v[74:77], v[212:215], v[200:203], v[74:77] cbsz:4 blgp:4
	v_mfma_f32_16x16x128_f8f6f4 v[74:77], v[220:223], v[208:211], v[74:77] cbsz:4 blgp:4
	v_mfma_f32_16x16x128_f8f6f4 v[78:81], v[216:219], v[200:203], v[78:81] cbsz:4 blgp:4
	v_mfma_f32_16x16x128_f8f6f4 v[78:81], v[224:227], v[208:211], v[78:81] cbsz:4 blgp:4
	s_barrier
	s_mov_b32 m0, s65
	s_nop 0
	global_load_lds_dwordx4 v148, s[44:45]
	s_mov_b32 m0, s66
	s_nop 0
	global_load_lds_dwordx4 v152, s[44:45]
	ds_read_b128 v[180:183], v165 offset:49152
	ds_read_b128 v[184:187], v165 offset:51200
	ds_read_b128 v[188:191], v166 offset:49152
	ds_read_b128 v[192:195], v166 offset:51200
	ds_read_b128 v[196:199], v165 offset:53248
	ds_read_b128 v[200:203], v165 offset:55296
	ds_read_b128 v[204:207], v166 offset:53248
	ds_read_b128 v[208:211], v166 offset:55296
	s_mov_b32 m0, s67
	s_nop 0
	global_load_lds_dwordx4 v146, s[46:47]
	s_mov_b32 m0, s68
	s_nop 0
	global_load_lds_dwordx4 v150, s[46:47]
	s_add_u32 s44, s44, s24
	s_addc_u32 s45, s45, s25
	s_mov_b32 m0, s69
	s_nop 0
	global_load_lds_dwordx4 v148, s[44:45]
	s_mov_b32 m0, s70
	s_nop 0
	global_load_lds_dwordx4 v152, s[44:45]
	s_waitcnt vmcnt(8)
	s_waitcnt lgkmcnt(0)
	s_barrier
	v_mfma_f32_16x16x128_f8f6f4 v[86:89], v[156:159], v[180:183], v[86:89] cbsz:4 blgp:4
	v_mfma_f32_16x16x128_f8f6f4 v[86:89], v[172:175], v[188:191], v[86:89] cbsz:4 blgp:4
	v_mfma_f32_16x16x128_f8f6f4 v[90:93], v[168:171], v[180:183], v[90:93] cbsz:4 blgp:4
	v_mfma_f32_16x16x128_f8f6f4 v[90:93], v[176:179], v[188:191], v[90:93] cbsz:4 blgp:4
	v_mfma_f32_16x16x128_f8f6f4 v[98:101], v[156:159], v[184:187], v[98:101] cbsz:4 blgp:4
	v_mfma_f32_16x16x128_f8f6f4 v[98:101], v[172:175], v[192:195], v[98:101] cbsz:4 blgp:4
	v_mfma_f32_16x16x128_f8f6f4 v[106:109], v[168:171], v[184:187], v[106:109] cbsz:4 blgp:4
	v_mfma_f32_16x16x128_f8f6f4 v[106:109], v[176:179], v[192:195], v[106:109] cbsz:4 blgp:4
	v_mfma_f32_16x16x128_f8f6f4 v[118:121], v[156:159], v[196:199], v[118:121] cbsz:4 blgp:4
	v_mfma_f32_16x16x128_f8f6f4 v[118:121], v[172:175], v[204:207], v[118:121] cbsz:4 blgp:4
	v_mfma_f32_16x16x128_f8f6f4 v[126:129], v[168:171], v[196:199], v[126:129] cbsz:4 blgp:4
	v_mfma_f32_16x16x128_f8f6f4 v[126:129], v[176:179], v[204:207], v[126:129] cbsz:4 blgp:4
	v_mfma_f32_16x16x128_f8f6f4 v[138:141], v[156:159], v[200:203], v[138:141] cbsz:4 blgp:4
	v_mfma_f32_16x16x128_f8f6f4 v[138:141], v[172:175], v[208:211], v[138:141] cbsz:4 blgp:4
	v_mfma_f32_16x16x128_f8f6f4 v[82:85], v[168:171], v[200:203], v[82:85] cbsz:4 blgp:4
	v_mfma_f32_16x16x128_f8f6f4 v[82:85], v[176:179], v[208:211], v[82:85] cbsz:4 blgp:4
	v_mfma_f32_16x16x128_f8f6f4 v[94:97], v[212:215], v[180:183], v[94:97] cbsz:4 blgp:4
	v_mfma_f32_16x16x128_f8f6f4 v[94:97], v[220:223], v[188:191], v[94:97] cbsz:4 blgp:4
	v_mfma_f32_16x16x128_f8f6f4 v[102:105], v[216:219], v[180:183], v[102:105] cbsz:4 blgp:4
	v_mfma_f32_16x16x128_f8f6f4 v[102:105], v[224:227], v[188:191], v[102:105] cbsz:4 blgp:4
	v_mfma_f32_16x16x128_f8f6f4 v[110:113], v[212:215], v[184:187], v[110:113] cbsz:4 blgp:4
	v_mfma_f32_16x16x128_f8f6f4 v[110:113], v[220:223], v[192:195], v[110:113] cbsz:4 blgp:4
	v_mfma_f32_16x16x128_f8f6f4 v[114:117], v[216:219], v[184:187], v[114:117] cbsz:4 blgp:4
	v_mfma_f32_16x16x128_f8f6f4 v[114:117], v[224:227], v[192:195], v[114:117] cbsz:4 blgp:4
	v_mfma_f32_16x16x128_f8f6f4 v[122:125], v[212:215], v[196:199], v[122:125] cbsz:4 blgp:4
	v_mfma_f32_16x16x128_f8f6f4 v[122:125], v[220:223], v[204:207], v[122:125] cbsz:4 blgp:4
	v_mfma_f32_16x16x128_f8f6f4 v[130:133], v[216:219], v[196:199], v[130:133] cbsz:4 blgp:4
	v_mfma_f32_16x16x128_f8f6f4 v[130:133], v[224:227], v[204:207], v[130:133] cbsz:4 blgp:4
	v_mfma_f32_16x16x128_f8f6f4 v[134:137], v[212:215], v[200:203], v[134:137] cbsz:4 blgp:4
	v_mfma_f32_16x16x128_f8f6f4 v[134:137], v[220:223], v[208:211], v[134:137] cbsz:4 blgp:4
	v_mfma_f32_16x16x128_f8f6f4 v[142:145], v[216:219], v[200:203], v[142:145] cbsz:4 blgp:4
	v_mfma_f32_16x16x128_f8f6f4 v[142:145], v[224:227], v[208:211], v[142:145] cbsz:4 blgp:4
	s_andn2_b64 vcc, exec, s[34:35]
	s_barrier
	s_cbranch_vccnz .LBB5_4
	s_ashr_i32 s29, s28, 31
	s_lshl_b64 s[44:45], s[28:29], 10
	s_add_u32 s44, s10, s44
	s_addc_u32 s45, s11, s45
	s_add_u32 s29, s42, 0x200
	s_addc_u32 s79, s43, 0
	s_add_u32 s80, s40, 0x200
	s_addc_u32 s81, s41, 0
	s_add_u32 s40, s82, 0x180
	s_addc_u32 s41, s83, 0
	s_mov_b32 s82, 4
	s_cmp_eq_u32 s64, s82
	s_cselect_b64 s[42:43], -1, 0
	s_cmp_lg_u32 s64, s82
	s_cbranch_scc1 .LBB5_15

.LBB5_15:
	ds_read_b128 v[156:159], v163
	ds_read_b128 v[168:171], v163 offset:2048
	ds_read_b128 v[172:175], v164
	ds_read_b128 v[176:179], v164 offset:2048
	s_and_b64 s[42:43], s[42:43], exec
	s_cselect_b32 s48, s38, s29
	s_cselect_b32 s49, s39, s79
	s_cselect_b32 s51, s5, s81
	s_cselect_b32 s50, s4, s80
	s_add_u32 s46, s48, 0x80
	s_addc_u32 s47, s49, 0
	s_add_u32 s42, s50, 0x80
	s_addc_u32 s43, s51, 0
	ds_read_b128 v[180:183], v165
	ds_read_b128 v[184:187], v165 offset:2048
	ds_read_b128 v[188:191], v166
	ds_read_b128 v[192:195], v166 offset:2048
	ds_read_b128 v[196:199], v165 offset:4096
	ds_read_b128 v[200:203], v165 offset:6144
	ds_read_b128 v[204:207], v166 offset:4096
	ds_read_b128 v[208:211], v166 offset:6144
	s_mov_b32 m0, s71
	s_nop 0
	global_load_lds_dwordx4 v146, s[40:41]
	s_mov_b32 m0, s72
	s_nop 0
	global_load_lds_dwordx4 v150, s[40:41]
	s_waitcnt lgkmcnt(8)
	ds_read_b128 v[212:215], v163 offset:16384
	ds_read_b128 v[216:219], v163 offset:18432
	ds_read_b128 v[220:223], v164 offset:16384
	ds_read_b128 v[224:227], v164 offset:18432
	s_waitcnt vmcnt(8)
	s_waitcnt lgkmcnt(0)
	s_barrier
	s_waitcnt lgkmcnt(0)
	v_mfma_f32_16x16x128_f8f6f4 v[18:21], v[156:159], v[180:183], v[18:21] cbsz:4 blgp:4
	v_mfma_f32_16x16x128_f8f6f4 v[18:21], v[172:175], v[188:191], v[18:21] cbsz:4 blgp:4
	v_mfma_f32_16x16x128_f8f6f4 v[22:25], v[168:171], v[180:183], v[22:25] cbsz:4 blgp:4
	v_mfma_f32_16x16x128_f8f6f4 v[22:25], v[176:179], v[188:191], v[22:25] cbsz:4 blgp:4
	v_mfma_f32_16x16x128_f8f6f4 v[26:29], v[156:159], v[184:187], v[26:29] cbsz:4 blgp:4
	v_mfma_f32_16x16x128_f8f6f4 v[26:29], v[172:175], v[192:195], v[26:29] cbsz:4 blgp:4
	v_mfma_f32_16x16x128_f8f6f4 v[30:33], v[168:171], v[184:187], v[30:33] cbsz:4 blgp:4
	v_mfma_f32_16x16x128_f8f6f4 v[30:33], v[176:179], v[192:195], v[30:33] cbsz:4 blgp:4
	v_mfma_f32_16x16x128_f8f6f4 v[34:37], v[156:159], v[196:199], v[34:37] cbsz:4 blgp:4
	v_mfma_f32_16x16x128_f8f6f4 v[34:37], v[172:175], v[204:207], v[34:37] cbsz:4 blgp:4
	v_mfma_f32_16x16x128_f8f6f4 v[38:41], v[168:171], v[196:199], v[38:41] cbsz:4 blgp:4
	v_mfma_f32_16x16x128_f8f6f4 v[38:41], v[176:179], v[204:207], v[38:41] cbsz:4 blgp:4
	v_mfma_f32_16x16x128_f8f6f4 v[42:45], v[156:159], v[200:203], v[42:45] cbsz:4 blgp:4
	v_mfma_f32_16x16x128_f8f6f4 v[42:45], v[172:175], v[208:211], v[42:45] cbsz:4 blgp:4
	v_mfma_f32_16x16x128_f8f6f4 v[46:49], v[168:171], v[200:203], v[46:49] cbsz:4 blgp:4
	v_mfma_f32_16x16x128_f8f6f4 v[46:49], v[176:179], v[208:211], v[46:49] cbsz:4 blgp:4
	v_mfma_f32_16x16x128_f8f6f4 v[50:53], v[212:215], v[180:183], v[50:53] cbsz:4 blgp:4
	v_mfma_f32_16x16x128_f8f6f4 v[50:53], v[220:223], v[188:191], v[50:53] cbsz:4 blgp:4
	v_mfma_f32_16x16x128_f8f6f4 v[54:57], v[216:219], v[180:183], v[54:57] cbsz:4 blgp:4
	v_mfma_f32_16x16x128_f8f6f4 v[54:57], v[224:227], v[188:191], v[54:57] cbsz:4 blgp:4
	v_mfma_f32_16x16x128_f8f6f4 v[58:61], v[212:215], v[184:187], v[58:61] cbsz:4 blgp:4
	v_mfma_f32_16x16x128_f8f6f4 v[58:61], v[220:223], v[192:195], v[58:61] cbsz:4 blgp:4
	v_mfma_f32_16x16x128_f8f6f4 v[62:65], v[216:219], v[184:187], v[62:65] cbsz:4 blgp:4
	v_mfma_f32_16x16x128_f8f6f4 v[62:65], v[224:227], v[192:195], v[62:65] cbsz:4 blgp:4
	v_mfma_f32_16x16x128_f8f6f4 v[66:69], v[212:215], v[196:199], v[66:69] cbsz:4 blgp:4
	v_mfma_f32_16x16x128_f8f6f4 v[66:69], v[220:223], v[204:207], v[66:69] cbsz:4 blgp:4
	v_mfma_f32_16x16x128_f8f6f4 v[70:73], v[216:219], v[196:199], v[70:73] cbsz:4 blgp:4
	v_mfma_f32_16x16x128_f8f6f4 v[70:73], v[224:227], v[204:207], v[70:73] cbsz:4 blgp:4
	v_mfma_f32_16x16x128_f8f6f4 v[74:77], v[212:215], v[200:203], v[74:77] cbsz:4 blgp:4
	v_mfma_f32_16x16x128_f8f6f4 v[74:77], v[220:223], v[208:211], v[74:77] cbsz:4 blgp:4
	v_mfma_f32_16x16x128_f8f6f4 v[78:81], v[216:219], v[200:203], v[78:81] cbsz:4 blgp:4
	v_mfma_f32_16x16x128_f8f6f4 v[78:81], v[224:227], v[208:211], v[78:81] cbsz:4 blgp:4
	s_barrier
	s_mov_b32 m0, s56
	s_nop 0
	global_load_lds_dwordx4 v148, s[50:51]
	s_mov_b32 m0, s57
	s_nop 0
	global_load_lds_dwordx4 v152, s[50:51]
	ds_read_b128 v[180:183], v165 offset:16384
	ds_read_b128 v[184:187], v165 offset:18432
	ds_read_b128 v[188:191], v166 offset:16384
	ds_read_b128 v[192:195], v166 offset:18432
	ds_read_b128 v[196:199], v165 offset:20480
	ds_read_b128 v[200:203], v165 offset:22528
	ds_read_b128 v[204:207], v166 offset:20480
	ds_read_b128 v[208:211], v166 offset:22528
	s_mov_b32 m0, s55
	s_nop 0
	global_load_lds_dwordx4 v146, s[48:49]
	s_mov_b32 m0, s58
	s_nop 0
	global_load_lds_dwordx4 v150, s[48:49]
	s_add_u32 s50, s50, s24
	s_addc_u32 s51, s51, s25
	s_mov_b32 m0, s59
	s_nop 0
	global_load_lds_dwordx4 v148, s[50:51]
	s_mov_b32 m0, s60
	s_nop 0
	global_load_lds_dwordx4 v152, s[50:51]
	s_waitcnt vmcnt(8)
	s_waitcnt lgkmcnt(0)
	s_barrier
	v_mfma_f32_16x16x128_f8f6f4 v[86:89], v[156:159], v[180:183], v[86:89] cbsz:4 blgp:4
	v_mfma_f32_16x16x128_f8f6f4 v[86:89], v[172:175], v[188:191], v[86:89] cbsz:4 blgp:4
	v_mfma_f32_16x16x128_f8f6f4 v[90:93], v[168:171], v[180:183], v[90:93] cbsz:4 blgp:4
	v_mfma_f32_16x16x128_f8f6f4 v[90:93], v[176:179], v[188:191], v[90:93] cbsz:4 blgp:4
	v_mfma_f32_16x16x128_f8f6f4 v[98:101], v[156:159], v[184:187], v[98:101] cbsz:4 blgp:4
	v_mfma_f32_16x16x128_f8f6f4 v[98:101], v[172:175], v[192:195], v[98:101] cbsz:4 blgp:4
	v_mfma_f32_16x16x128_f8f6f4 v[106:109], v[168:171], v[184:187], v[106:109] cbsz:4 blgp:4
	v_mfma_f32_16x16x128_f8f6f4 v[106:109], v[176:179], v[192:195], v[106:109] cbsz:4 blgp:4
	v_mfma_f32_16x16x128_f8f6f4 v[118:121], v[156:159], v[196:199], v[118:121] cbsz:4 blgp:4
	v_mfma_f32_16x16x128_f8f6f4 v[118:121], v[172:175], v[204:207], v[118:121] cbsz:4 blgp:4
	v_mfma_f32_16x16x128_f8f6f4 v[126:129], v[168:171], v[196:199], v[126:129] cbsz:4 blgp:4
	v_mfma_f32_16x16x128_f8f6f4 v[126:129], v[176:179], v[204:207], v[126:129] cbsz:4 blgp:4
	v_mfma_f32_16x16x128_f8f6f4 v[138:141], v[156:159], v[200:203], v[138:141] cbsz:4 blgp:4
	v_mfma_f32_16x16x128_f8f6f4 v[138:141], v[172:175], v[208:211], v[138:141] cbsz:4 blgp:4
	v_mfma_f32_16x16x128_f8f6f4 v[82:85], v[168:171], v[200:203], v[82:85] cbsz:4 blgp:4
	v_mfma_f32_16x16x128_f8f6f4 v[82:85], v[176:179], v[208:211], v[82:85] cbsz:4 blgp:4
	v_mfma_f32_16x16x128_f8f6f4 v[94:97], v[212:215], v[180:183], v[94:97] cbsz:4 blgp:4
	v_mfma_f32_16x16x128_f8f6f4 v[94:97], v[220:223], v[188:191], v[94:97] cbsz:4 blgp:4
	v_mfma_f32_16x16x128_f8f6f4 v[102:105], v[216:219], v[180:183], v[102:105] cbsz:4 blgp:4
	v_mfma_f32_16x16x128_f8f6f4 v[102:105], v[224:227], v[188:191], v[102:105] cbsz:4 blgp:4
	v_mfma_f32_16x16x128_f8f6f4 v[110:113], v[212:215], v[184:187], v[110:113] cbsz:4 blgp:4
	v_mfma_f32_16x16x128_f8f6f4 v[110:113], v[220:223], v[192:195], v[110:113] cbsz:4 blgp:4
	v_mfma_f32_16x16x128_f8f6f4 v[114:117], v[216:219], v[184:187], v[114:117] cbsz:4 blgp:4
	v_mfma_f32_16x16x128_f8f6f4 v[114:117], v[224:227], v[192:195], v[114:117] cbsz:4 blgp:4
	v_mfma_f32_16x16x128_f8f6f4 v[122:125], v[212:215], v[196:199], v[122:125] cbsz:4 blgp:4
	v_mfma_f32_16x16x128_f8f6f4 v[122:125], v[220:223], v[204:207], v[122:125] cbsz:4 blgp:4
	v_mfma_f32_16x16x128_f8f6f4 v[130:133], v[216:219], v[196:199], v[130:133] cbsz:4 blgp:4
	v_mfma_f32_16x16x128_f8f6f4 v[130:133], v[224:227], v[204:207], v[130:133] cbsz:4 blgp:4
	v_mfma_f32_16x16x128_f8f6f4 v[134:137], v[212:215], v[200:203], v[134:137] cbsz:4 blgp:4
	v_mfma_f32_16x16x128_f8f6f4 v[134:137], v[220:223], v[208:211], v[134:137] cbsz:4 blgp:4
	v_mfma_f32_16x16x128_f8f6f4 v[142:145], v[216:219], v[200:203], v[142:145] cbsz:4 blgp:4
	v_mfma_f32_16x16x128_f8f6f4 v[142:145], v[224:227], v[208:211], v[142:145] cbsz:4 blgp:4
	s_barrier
	ds_read_b128 v[156:159], v163 offset:32768
	ds_read_b128 v[168:171], v163 offset:34816
	ds_read_b128 v[172:175], v164 offset:32768
	ds_read_b128 v[176:179], v164 offset:34816
	ds_read_b128 v[180:183], v165 offset:32768
	ds_read_b128 v[184:187], v165 offset:34816
	ds_read_b128 v[188:191], v166 offset:32768
	ds_read_b128 v[192:195], v166 offset:34816
	ds_read_b128 v[196:199], v165 offset:36864
	ds_read_b128 v[200:203], v165 offset:38912
	ds_read_b128 v[204:207], v166 offset:36864
	ds_read_b128 v[208:211], v166 offset:38912
	s_add_u32 s48, s48, s22
	s_addc_u32 s49, s49, s23
	s_mov_b32 m0, s61
	s_nop 0
	global_load_lds_dwordx4 v146, s[48:49]
	s_mov_b32 m0, s62
	s_nop 0
	global_load_lds_dwordx4 v150, s[48:49]
	s_waitcnt lgkmcnt(8)
	ds_read_b128 v[212:215], v163 offset:49152
	ds_read_b128 v[216:219], v163 offset:51200
	ds_read_b128 v[220:223], v164 offset:49152
	ds_read_b128 v[224:227], v164 offset:51200
	s_waitcnt vmcnt(8)
	s_waitcnt lgkmcnt(0)
	s_barrier
	s_waitcnt lgkmcnt(0)
	v_mfma_f32_16x16x128_f8f6f4 v[18:21], v[156:159], v[180:183], v[18:21] cbsz:4 blgp:4
	v_mfma_f32_16x16x128_f8f6f4 v[18:21], v[172:175], v[188:191], v[18:21] cbsz:4 blgp:4
	v_mfma_f32_16x16x128_f8f6f4 v[22:25], v[168:171], v[180:183], v[22:25] cbsz:4 blgp:4
	v_mfma_f32_16x16x128_f8f6f4 v[22:25], v[176:179], v[188:191], v[22:25] cbsz:4 blgp:4
	v_mfma_f32_16x16x128_f8f6f4 v[26:29], v[156:159], v[184:187], v[26:29] cbsz:4 blgp:4
	v_mfma_f32_16x16x128_f8f6f4 v[26:29], v[172:175], v[192:195], v[26:29] cbsz:4 blgp:4
	v_mfma_f32_16x16x128_f8f6f4 v[30:33], v[168:171], v[184:187], v[30:33] cbsz:4 blgp:4
	v_mfma_f32_16x16x128_f8f6f4 v[30:33], v[176:179], v[192:195], v[30:33] cbsz:4 blgp:4
	v_mfma_f32_16x16x128_f8f6f4 v[34:37], v[156:159], v[196:199], v[34:37] cbsz:4 blgp:4
	v_mfma_f32_16x16x128_f8f6f4 v[34:37], v[172:175], v[204:207], v[34:37] cbsz:4 blgp:4
	v_mfma_f32_16x16x128_f8f6f4 v[38:41], v[168:171], v[196:199], v[38:41] cbsz:4 blgp:4
	v_mfma_f32_16x16x128_f8f6f4 v[38:41], v[176:179], v[204:207], v[38:41] cbsz:4 blgp:4
	v_mfma_f32_16x16x128_f8f6f4 v[42:45], v[156:159], v[200:203], v[42:45] cbsz:4 blgp:4
	v_mfma_f32_16x16x128_f8f6f4 v[42:45], v[172:175], v[208:211], v[42:45] cbsz:4 blgp:4
	v_mfma_f32_16x16x128_f8f6f4 v[46:49], v[168:171], v[200:203], v[46:49] cbsz:4 blgp:4
	v_mfma_f32_16x16x128_f8f6f4 v[46:49], v[176:179], v[208:211], v[46:49] cbsz:4 blgp:4
	v_mfma_f32_16x16x128_f8f6f4 v[50:53], v[212:215], v[180:183], v[50:53] cbsz:4 blgp:4
	v_mfma_f32_16x16x128_f8f6f4 v[50:53], v[220:223], v[188:191], v[50:53] cbsz:4 blgp:4
	v_mfma_f32_16x16x128_f8f6f4 v[54:57], v[216:219], v[180:183], v[54:57] cbsz:4 blgp:4
	v_mfma_f32_16x16x128_f8f6f4 v[54:57], v[224:227], v[188:191], v[54:57] cbsz:4 blgp:4
	v_mfma_f32_16x16x128_f8f6f4 v[58:61], v[212:215], v[184:187], v[58:61] cbsz:4 blgp:4
	v_mfma_f32_16x16x128_f8f6f4 v[58:61], v[220:223], v[192:195], v[58:61] cbsz:4 blgp:4
	v_mfma_f32_16x16x128_f8f6f4 v[62:65], v[216:219], v[184:187], v[62:65] cbsz:4 blgp:4
	v_mfma_f32_16x16x128_f8f6f4 v[62:65], v[224:227], v[192:195], v[62:65] cbsz:4 blgp:4
	v_mfma_f32_16x16x128_f8f6f4 v[66:69], v[212:215], v[196:199], v[66:69] cbsz:4 blgp:4
	v_mfma_f32_16x16x128_f8f6f4 v[66:69], v[220:223], v[204:207], v[66:69] cbsz:4 blgp:4
	v_mfma_f32_16x16x128_f8f6f4 v[70:73], v[216:219], v[196:199], v[70:73] cbsz:4 blgp:4
	v_mfma_f32_16x16x128_f8f6f4 v[70:73], v[224:227], v[204:207], v[70:73] cbsz:4 blgp:4
	v_mfma_f32_16x16x128_f8f6f4 v[74:77], v[212:215], v[200:203], v[74:77] cbsz:4 blgp:4
	v_mfma_f32_16x16x128_f8f6f4 v[74:77], v[220:223], v[208:211], v[74:77] cbsz:4 blgp:4
	v_mfma_f32_16x16x128_f8f6f4 v[78:81], v[216:219], v[200:203], v[78:81] cbsz:4 blgp:4
	v_mfma_f32_16x16x128_f8f6f4 v[78:81], v[224:227], v[208:211], v[78:81] cbsz:4 blgp:4
	s_barrier
	s_mov_b32 m0, s65
	s_nop 0
	global_load_lds_dwordx4 v148, s[42:43]
	s_mov_b32 m0, s66
	s_nop 0
	global_load_lds_dwordx4 v152, s[42:43]
	ds_read_b128 v[180:183], v165 offset:49152
	ds_read_b128 v[184:187], v165 offset:51200
	ds_read_b128 v[188:191], v166 offset:49152
	ds_read_b128 v[192:195], v166 offset:51200
	ds_read_b128 v[196:199], v165 offset:53248
	ds_read_b128 v[200:203], v165 offset:55296
	ds_read_b128 v[204:207], v166 offset:53248
	ds_read_b128 v[208:211], v166 offset:55296
	s_mov_b32 m0, s67
	s_nop 0
	global_load_lds_dwordx4 v146, s[46:47]
	s_mov_b32 m0, s68
	s_nop 0
	global_load_lds_dwordx4 v150, s[46:47]
	s_add_u32 s42, s42, s24
	s_addc_u32 s43, s43, s25
	s_mov_b32 m0, s69
	s_nop 0
	global_load_lds_dwordx4 v148, s[42:43]
	s_mov_b32 m0, s70
	s_nop 0
	global_load_lds_dwordx4 v152, s[42:43]
	s_waitcnt vmcnt(8)
	s_waitcnt lgkmcnt(0)
	s_barrier
	v_mfma_f32_16x16x128_f8f6f4 v[86:89], v[156:159], v[180:183], v[86:89] cbsz:4 blgp:4
	v_mfma_f32_16x16x128_f8f6f4 v[86:89], v[172:175], v[188:191], v[86:89] cbsz:4 blgp:4
	v_mfma_f32_16x16x128_f8f6f4 v[90:93], v[168:171], v[180:183], v[90:93] cbsz:4 blgp:4
	v_mfma_f32_16x16x128_f8f6f4 v[90:93], v[176:179], v[188:191], v[90:93] cbsz:4 blgp:4
	v_mfma_f32_16x16x128_f8f6f4 v[98:101], v[156:159], v[184:187], v[98:101] cbsz:4 blgp:4
	v_mfma_f32_16x16x128_f8f6f4 v[98:101], v[172:175], v[192:195], v[98:101] cbsz:4 blgp:4
	v_mfma_f32_16x16x128_f8f6f4 v[106:109], v[168:171], v[184:187], v[106:109] cbsz:4 blgp:4
	v_mfma_f32_16x16x128_f8f6f4 v[106:109], v[176:179], v[192:195], v[106:109] cbsz:4 blgp:4
	v_mfma_f32_16x16x128_f8f6f4 v[118:121], v[156:159], v[196:199], v[118:121] cbsz:4 blgp:4
	v_mfma_f32_16x16x128_f8f6f4 v[118:121], v[172:175], v[204:207], v[118:121] cbsz:4 blgp:4
	v_mfma_f32_16x16x128_f8f6f4 v[126:129], v[168:171], v[196:199], v[126:129] cbsz:4 blgp:4
	v_mfma_f32_16x16x128_f8f6f4 v[126:129], v[176:179], v[204:207], v[126:129] cbsz:4 blgp:4
	v_mfma_f32_16x16x128_f8f6f4 v[138:141], v[156:159], v[200:203], v[138:141] cbsz:4 blgp:4
	v_mfma_f32_16x16x128_f8f6f4 v[138:141], v[172:175], v[208:211], v[138:141] cbsz:4 blgp:4
	v_mfma_f32_16x16x128_f8f6f4 v[82:85], v[168:171], v[200:203], v[82:85] cbsz:4 blgp:4
	v_mfma_f32_16x16x128_f8f6f4 v[82:85], v[176:179], v[208:211], v[82:85] cbsz:4 blgp:4
	v_mfma_f32_16x16x128_f8f6f4 v[94:97], v[212:215], v[180:183], v[94:97] cbsz:4 blgp:4
	v_mfma_f32_16x16x128_f8f6f4 v[94:97], v[220:223], v[188:191], v[94:97] cbsz:4 blgp:4
	v_mfma_f32_16x16x128_f8f6f4 v[102:105], v[216:219], v[180:183], v[102:105] cbsz:4 blgp:4
	v_mfma_f32_16x16x128_f8f6f4 v[102:105], v[224:227], v[188:191], v[102:105] cbsz:4 blgp:4
	v_mfma_f32_16x16x128_f8f6f4 v[110:113], v[212:215], v[184:187], v[110:113] cbsz:4 blgp:4
	v_mfma_f32_16x16x128_f8f6f4 v[110:113], v[220:223], v[192:195], v[110:113] cbsz:4 blgp:4
	v_mfma_f32_16x16x128_f8f6f4 v[114:117], v[216:219], v[184:187], v[114:117] cbsz:4 blgp:4
	v_mfma_f32_16x16x128_f8f6f4 v[114:117], v[224:227], v[192:195], v[114:117] cbsz:4 blgp:4
	v_mfma_f32_16x16x128_f8f6f4 v[122:125], v[212:215], v[196:199], v[122:125] cbsz:4 blgp:4
	v_mfma_f32_16x16x128_f8f6f4 v[122:125], v[220:223], v[204:207], v[122:125] cbsz:4 blgp:4
	v_mfma_f32_16x16x128_f8f6f4 v[130:133], v[216:219], v[196:199], v[130:133] cbsz:4 blgp:4
	v_mfma_f32_16x16x128_f8f6f4 v[130:133], v[224:227], v[204:207], v[130:133] cbsz:4 blgp:4
	v_mfma_f32_16x16x128_f8f6f4 v[134:137], v[212:215], v[200:203], v[134:137] cbsz:4 blgp:4
	v_mfma_f32_16x16x128_f8f6f4 v[134:137], v[220:223], v[208:211], v[134:137] cbsz:4 blgp:4
	v_mfma_f32_16x16x128_f8f6f4 v[142:145], v[216:219], v[200:203], v[142:145] cbsz:4 blgp:4
	v_mfma_f32_16x16x128_f8f6f4 v[142:145], v[224:227], v[208:211], v[142:145] cbsz:4 blgp:4
	s_add_i32 s42, s82, 2
	s_add_u32 s29, s29, 0x100
	s_addc_u32 s79, s79, 0
	s_add_u32 s80, s80, 0x100
	s_addc_u32 s81, s81, 0
	s_add_u32 s40, s40, 0x100
	s_addc_u32 s41, s41, 0
	s_cmp_ge_i32 s82, s64
	s_barrier
	s_cbranch_scc1 .LBB5_4
	s_mov_b32 s82, s42
	s_cmp_eq_u32 s64, s82
	s_cselect_b64 s[42:43], -1, 0
	s_cmp_lg_u32 s64, s82
	s_cbranch_scc0 .LBB5_14
	s_branch .LBB5_15

.LBB6_15:
	s_add_u32 s82, s36, s20
	s_addc_u32 s83, s37, s21
	s_add_u32 s31, s36, 0x100
	s_addc_u32 s39, s37, 0
	s_and_b64 s[40:41], s[12:13], exec
	ds_read_b128 v[82:85], v169
	ds_read_b128 v[94:97], v169 offset:2048
	ds_read_b128 v[102:105], v178
	ds_read_b128 v[110:113], v178 offset:2048
	s_cselect_b32 s45, s5, s39
	s_cselect_b32 s44, s4, s31
	s_add_u32 s31, s34, 0x100
	s_addc_u32 s39, s35, 0
	s_and_b64 s[40:41], s[12:13], exec
	s_cselect_b32 s47, s7, s39
	s_cselect_b32 s46, s6, s31
	s_add_u32 s42, s44, 0x80
	s_addc_u32 s43, s45, 0
	s_add_u32 s40, s46, 0x80
	s_addc_u32 s41, s47, 0
	ds_read_b128 v[58:61], v179
	ds_read_b128 v[66:69], v179 offset:2048
	ds_read_b128 v[62:65], v180
	ds_read_b128 v[70:73], v180 offset:2048
	ds_read_b128 v[74:77], v179 offset:4096
	ds_read_b128 v[86:89], v179 offset:6144
	ds_read_b128 v[78:81], v180 offset:4096
	ds_read_b128 v[90:93], v180 offset:6144
	s_add_u32 s84, s82, 0x80
	s_addc_u32 s85, s83, 0
	s_mov_b32 m0, s68
	s_nop 0
	global_load_lds_dwordx4 v162, s[84:85]
	s_mov_b32 m0, s69
	s_nop 0
	global_load_lds_dwordx4 v166, s[84:85]
	s_waitcnt lgkmcnt(8)
	ds_read_b128 v[142:145], v169 offset:16384
	ds_read_b128 v[146:149], v169 offset:18432
	ds_read_b128 v[150:153], v178 offset:16384
	ds_read_b128 v[154:157], v178 offset:18432
	s_waitcnt vmcnt(8)
	s_waitcnt lgkmcnt(0)
	s_barrier
	s_waitcnt lgkmcnt(0)
	s_waitcnt vmcnt(16)
	v_mov_b32_e32 v171, v170
	v_pk_mul_f32 v[16:17], v[170:171], v[16:17]
	v_pk_mul_f32 v[14:15], v[172:173], v[14:15]
	v_pk_mul_f32 v[12:13], v[170:171], v[12:13]
	v_pk_mul_f32 v[10:11], v[172:173], v[10:11]
	v_pk_mul_f32 v[8:9], v[170:171], v[8:9]
	v_pk_mul_f32 v[6:7], v[172:173], v[6:7]
	v_pk_mul_f32 v[4:5], v[170:171], v[4:5]
	v_pk_mul_f32 v[2:3], v[172:173], v[2:3]
	v_mfma_f32_16x16x128_f8f6f4 v[18:21], v[82:85], v[58:61], v[14:17] cbsz:4 blgp:4
	v_mfma_f32_16x16x128_f8f6f4 v[18:21], v[102:105], v[62:65], v[18:21] cbsz:4 blgp:4
	v_mfma_f32_16x16x128_f8f6f4 v[22:25], v[94:97], v[58:61], v[10:13] cbsz:4 blgp:4
	v_mfma_f32_16x16x128_f8f6f4 v[22:25], v[110:113], v[62:65], v[22:25] cbsz:4 blgp:4
	v_mfma_f32_16x16x128_f8f6f4 v[26:29], v[82:85], v[66:69], v[14:17] cbsz:4 blgp:4
	v_mfma_f32_16x16x128_f8f6f4 v[26:29], v[102:105], v[70:73], v[26:29] cbsz:4 blgp:4
	v_mfma_f32_16x16x128_f8f6f4 v[30:33], v[94:97], v[66:69], v[10:13] cbsz:4 blgp:4
	v_mfma_f32_16x16x128_f8f6f4 v[30:33], v[110:113], v[70:73], v[30:33] cbsz:4 blgp:4
	v_mfma_f32_16x16x128_f8f6f4 v[34:37], v[82:85], v[74:77], v[14:17] cbsz:4 blgp:4
	v_mfma_f32_16x16x128_f8f6f4 v[34:37], v[102:105], v[78:81], v[34:37] cbsz:4 blgp:4
	v_mfma_f32_16x16x128_f8f6f4 v[38:41], v[94:97], v[74:77], v[10:13] cbsz:4 blgp:4
	v_mfma_f32_16x16x128_f8f6f4 v[38:41], v[110:113], v[78:81], v[38:41] cbsz:4 blgp:4
	v_mfma_f32_16x16x128_f8f6f4 v[42:45], v[82:85], v[86:89], v[14:17] cbsz:4 blgp:4
	v_mfma_f32_16x16x128_f8f6f4 v[42:45], v[102:105], v[90:93], v[42:45] cbsz:4 blgp:4
	v_mfma_f32_16x16x128_f8f6f4 v[46:49], v[94:97], v[86:89], v[10:13] cbsz:4 blgp:4
	v_mfma_f32_16x16x128_f8f6f4 v[46:49], v[110:113], v[90:93], v[46:49] cbsz:4 blgp:4
	v_mfma_f32_16x16x128_f8f6f4 v[50:53], v[142:145], v[58:61], v[6:9] cbsz:4 blgp:4
	v_mfma_f32_16x16x128_f8f6f4 v[50:53], v[150:153], v[62:65], v[50:53] cbsz:4 blgp:4
	v_mfma_f32_16x16x128_f8f6f4 v[54:57], v[146:149], v[58:61], v[2:5] cbsz:4 blgp:4
	v_mfma_f32_16x16x128_f8f6f4 v[54:57], v[154:157], v[62:65], v[54:57] cbsz:4 blgp:4
	v_mfma_f32_16x16x128_f8f6f4 v[58:61], v[142:145], v[66:69], v[6:9] cbsz:4 blgp:4
	v_mfma_f32_16x16x128_f8f6f4 v[58:61], v[150:153], v[70:73], v[58:61] cbsz:4 blgp:4
	v_mfma_f32_16x16x128_f8f6f4 v[62:65], v[146:149], v[66:69], v[2:5] cbsz:4 blgp:4
	v_mfma_f32_16x16x128_f8f6f4 v[62:65], v[154:157], v[70:73], v[62:65] cbsz:4 blgp:4
	v_mfma_f32_16x16x128_f8f6f4 v[66:69], v[142:145], v[74:77], v[6:9] cbsz:4 blgp:4
	v_mfma_f32_16x16x128_f8f6f4 v[66:69], v[150:153], v[78:81], v[66:69] cbsz:4 blgp:4
	v_mfma_f32_16x16x128_f8f6f4 v[70:73], v[146:149], v[74:77], v[2:5] cbsz:4 blgp:4
	v_mfma_f32_16x16x128_f8f6f4 v[70:73], v[154:157], v[78:81], v[70:73] cbsz:4 blgp:4
	v_mfma_f32_16x16x128_f8f6f4 v[74:77], v[142:145], v[86:89], v[6:9] cbsz:4 blgp:4
	v_mfma_f32_16x16x128_f8f6f4 v[74:77], v[150:153], v[90:93], v[74:77] cbsz:4 blgp:4
	v_mfma_f32_16x16x128_f8f6f4 v[78:81], v[146:149], v[86:89], v[2:5] cbsz:4 blgp:4
	v_mfma_f32_16x16x128_f8f6f4 v[78:81], v[154:157], v[90:93], v[78:81] cbsz:4 blgp:4
	s_barrier
	s_mov_b32 m0, s54
	s_nop 0
	global_load_lds_dwordx4 v164, s[46:47]
	s_mov_b32 m0, s55
	s_nop 0
	global_load_lds_dwordx4 v168, s[46:47]
	ds_read_b128 v[114:117], v179 offset:16384
	ds_read_b128 v[122:125], v179 offset:18432
	ds_read_b128 v[130:133], v180 offset:16384
	ds_read_b128 v[134:137], v180 offset:18432
	ds_read_b128 v[158:161], v179 offset:20480
	ds_read_b128 v[182:185], v179 offset:22528
	ds_read_b128 v[186:189], v180 offset:20480
	ds_read_b128 v[190:193], v180 offset:22528
	s_mov_b32 m0, s53
	s_nop 0
	global_load_lds_dwordx4 v162, s[44:45]
	s_mov_b32 m0, s56
	s_nop 0
	global_load_lds_dwordx4 v166, s[44:45]
	s_add_u32 s46, s46, s22
	s_addc_u32 s47, s47, s23
	s_mov_b32 m0, s57
	s_nop 0
	global_load_lds_dwordx4 v164, s[46:47]
	s_mov_b32 m0, s58
	s_nop 0
	global_load_lds_dwordx4 v168, s[46:47]
	s_waitcnt vmcnt(8)
	s_waitcnt lgkmcnt(0)
	s_barrier
	v_mfma_f32_16x16x128_f8f6f4 v[86:89], v[82:85], v[114:117], v[14:17] cbsz:4 blgp:4
	v_mfma_f32_16x16x128_f8f6f4 v[86:89], v[102:105], v[130:133], v[86:89] cbsz:4 blgp:4
	v_mfma_f32_16x16x128_f8f6f4 v[90:93], v[94:97], v[114:117], v[10:13] cbsz:4 blgp:4
	v_mfma_f32_16x16x128_f8f6f4 v[90:93], v[110:113], v[130:133], v[90:93] cbsz:4 blgp:4
	v_mfma_f32_16x16x128_f8f6f4 v[98:101], v[82:85], v[122:125], v[14:17] cbsz:4 blgp:4
	v_mfma_f32_16x16x128_f8f6f4 v[98:101], v[102:105], v[134:137], v[98:101] cbsz:4 blgp:4
	v_mfma_f32_16x16x128_f8f6f4 v[106:109], v[94:97], v[122:125], v[10:13] cbsz:4 blgp:4
	v_mfma_f32_16x16x128_f8f6f4 v[106:109], v[110:113], v[134:137], v[106:109] cbsz:4 blgp:4
	v_mfma_f32_16x16x128_f8f6f4 v[118:121], v[82:85], v[158:161], v[14:17] cbsz:4 blgp:4
	v_mfma_f32_16x16x128_f8f6f4 v[118:121], v[102:105], v[186:189], v[118:121] cbsz:4 blgp:4
	v_mfma_f32_16x16x128_f8f6f4 v[126:129], v[94:97], v[158:161], v[10:13] cbsz:4 blgp:4
	v_mfma_f32_16x16x128_f8f6f4 v[126:129], v[110:113], v[186:189], v[126:129] cbsz:4 blgp:4
	v_mfma_f32_16x16x128_f8f6f4 v[138:141], v[82:85], v[182:185], v[14:17] cbsz:4 blgp:4
	v_mfma_f32_16x16x128_f8f6f4 v[138:141], v[102:105], v[190:193], v[138:141] cbsz:4 blgp:4
	v_mfma_f32_16x16x128_f8f6f4 v[82:85], v[94:97], v[182:185], v[10:13] cbsz:4 blgp:4
	v_mfma_f32_16x16x128_f8f6f4 v[82:85], v[110:113], v[190:193], v[82:85] cbsz:4 blgp:4
	v_mfma_f32_16x16x128_f8f6f4 v[94:97], v[142:145], v[114:117], v[6:9] cbsz:4 blgp:4
	v_mfma_f32_16x16x128_f8f6f4 v[94:97], v[150:153], v[130:133], v[94:97] cbsz:4 blgp:4
	v_mfma_f32_16x16x128_f8f6f4 v[102:105], v[146:149], v[114:117], v[2:5] cbsz:4 blgp:4
	v_mfma_f32_16x16x128_f8f6f4 v[102:105], v[154:157], v[130:133], v[102:105] cbsz:4 blgp:4
	v_mfma_f32_16x16x128_f8f6f4 v[110:113], v[142:145], v[122:125], v[6:9] cbsz:4 blgp:4
	v_mfma_f32_16x16x128_f8f6f4 v[110:113], v[150:153], v[134:137], v[110:113] cbsz:4 blgp:4
	v_mfma_f32_16x16x128_f8f6f4 v[114:117], v[146:149], v[122:125], v[2:5] cbsz:4 blgp:4
	v_mfma_f32_16x16x128_f8f6f4 v[114:117], v[154:157], v[134:137], v[114:117] cbsz:4 blgp:4
	v_mfma_f32_16x16x128_f8f6f4 v[122:125], v[142:145], v[158:161], v[6:9] cbsz:4 blgp:4
	v_mfma_f32_16x16x128_f8f6f4 v[122:125], v[150:153], v[186:189], v[122:125] cbsz:4 blgp:4
	v_mfma_f32_16x16x128_f8f6f4 v[130:133], v[146:149], v[158:161], v[2:5] cbsz:4 blgp:4
	v_mfma_f32_16x16x128_f8f6f4 v[130:133], v[154:157], v[186:189], v[130:133] cbsz:4 blgp:4
	v_mfma_f32_16x16x128_f8f6f4 v[134:137], v[142:145], v[182:185], v[6:9] cbsz:4 blgp:4
	v_mfma_f32_16x16x128_f8f6f4 v[134:137], v[150:153], v[190:193], v[134:137] cbsz:4 blgp:4
	v_mfma_f32_16x16x128_f8f6f4 v[142:145], v[146:149], v[182:185], v[2:5] cbsz:4 blgp:4
	v_mfma_f32_16x16x128_f8f6f4 v[142:145], v[154:157], v[190:193], v[142:145] cbsz:4 blgp:4
	s_barrier
	ds_read_b128 v[146:149], v169 offset:32768
	ds_read_b128 v[150:153], v169 offset:34816
	ds_read_b128 v[154:157], v178 offset:32768
	ds_read_b128 v[158:161], v178 offset:34816
	ds_read_b128 v[182:185], v179 offset:32768
	ds_read_b128 v[186:189], v179 offset:34816
	ds_read_b128 v[190:193], v180 offset:32768
	ds_read_b128 v[194:197], v180 offset:34816
	ds_read_b128 v[198:201], v179 offset:36864
	ds_read_b128 v[202:205], v179 offset:38912
	ds_read_b128 v[206:209], v180 offset:36864
	ds_read_b128 v[210:213], v180 offset:38912
	s_add_u32 s44, s44, s20
	s_addc_u32 s45, s45, s21
	s_mov_b32 m0, s59
	s_nop 0
	global_load_lds_dwordx4 v162, s[44:45]
	s_mov_b32 m0, s60
	s_nop 0
	global_load_lds_dwordx4 v166, s[44:45]
	s_waitcnt lgkmcnt(8)
	ds_read_b128 v[214:217], v169 offset:49152
	ds_read_b128 v[218:221], v169 offset:51200
	ds_read_b128 v[222:225], v178 offset:49152
	ds_read_b128 v[226:229], v178 offset:51200
	s_waitcnt vmcnt(8)
	s_waitcnt lgkmcnt(0)
	s_barrier
	s_waitcnt lgkmcnt(0)
	v_mfma_f32_16x16x128_f8f6f4 v[18:21], v[146:149], v[182:185], v[18:21] cbsz:4 blgp:4
	v_mfma_f32_16x16x128_f8f6f4 v[18:21], v[154:157], v[190:193], v[18:21] cbsz:4 blgp:4
	v_mfma_f32_16x16x128_f8f6f4 v[22:25], v[150:153], v[182:185], v[22:25] cbsz:4 blgp:4
	v_mfma_f32_16x16x128_f8f6f4 v[22:25], v[158:161], v[190:193], v[22:25] cbsz:4 blgp:4
	v_mfma_f32_16x16x128_f8f6f4 v[26:29], v[146:149], v[186:189], v[26:29] cbsz:4 blgp:4
	v_mfma_f32_16x16x128_f8f6f4 v[26:29], v[154:157], v[194:197], v[26:29] cbsz:4 blgp:4
	v_mfma_f32_16x16x128_f8f6f4 v[30:33], v[150:153], v[186:189], v[30:33] cbsz:4 blgp:4
	v_mfma_f32_16x16x128_f8f6f4 v[30:33], v[158:161], v[194:197], v[30:33] cbsz:4 blgp:4
	v_mfma_f32_16x16x128_f8f6f4 v[34:37], v[146:149], v[198:201], v[34:37] cbsz:4 blgp:4
	v_mfma_f32_16x16x128_f8f6f4 v[34:37], v[154:157], v[206:209], v[34:37] cbsz:4 blgp:4
	v_mfma_f32_16x16x128_f8f6f4 v[38:41], v[150:153], v[198:201], v[38:41] cbsz:4 blgp:4
	v_mfma_f32_16x16x128_f8f6f4 v[38:41], v[158:161], v[206:209], v[38:41] cbsz:4 blgp:4
	v_mfma_f32_16x16x128_f8f6f4 v[42:45], v[146:149], v[202:205], v[42:45] cbsz:4 blgp:4
	v_mfma_f32_16x16x128_f8f6f4 v[42:45], v[154:157], v[210:213], v[42:45] cbsz:4 blgp:4
	v_mfma_f32_16x16x128_f8f6f4 v[46:49], v[150:153], v[202:205], v[46:49] cbsz:4 blgp:4
	v_mfma_f32_16x16x128_f8f6f4 v[46:49], v[158:161], v[210:213], v[46:49] cbsz:4 blgp:4
	v_mfma_f32_16x16x128_f8f6f4 v[50:53], v[214:217], v[182:185], v[50:53] cbsz:4 blgp:4
	v_mfma_f32_16x16x128_f8f6f4 v[50:53], v[222:225], v[190:193], v[50:53] cbsz:4 blgp:4
	v_mfma_f32_16x16x128_f8f6f4 v[54:57], v[218:221], v[182:185], v[54:57] cbsz:4 blgp:4
	v_mfma_f32_16x16x128_f8f6f4 v[54:57], v[226:229], v[190:193], v[54:57] cbsz:4 blgp:4
	v_mfma_f32_16x16x128_f8f6f4 v[58:61], v[214:217], v[186:189], v[58:61] cbsz:4 blgp:4
	v_mfma_f32_16x16x128_f8f6f4 v[58:61], v[222:225], v[194:197], v[58:61] cbsz:4 blgp:4
	v_mfma_f32_16x16x128_f8f6f4 v[62:65], v[218:221], v[186:189], v[62:65] cbsz:4 blgp:4
	v_mfma_f32_16x16x128_f8f6f4 v[62:65], v[226:229], v[194:197], v[62:65] cbsz:4 blgp:4
	v_mfma_f32_16x16x128_f8f6f4 v[66:69], v[214:217], v[198:201], v[66:69] cbsz:4 blgp:4
	v_mfma_f32_16x16x128_f8f6f4 v[66:69], v[222:225], v[206:209], v[66:69] cbsz:4 blgp:4
	v_mfma_f32_16x16x128_f8f6f4 v[70:73], v[218:221], v[198:201], v[70:73] cbsz:4 blgp:4
	v_mfma_f32_16x16x128_f8f6f4 v[70:73], v[226:229], v[206:209], v[70:73] cbsz:4 blgp:4
	v_mfma_f32_16x16x128_f8f6f4 v[74:77], v[214:217], v[202:205], v[74:77] cbsz:4 blgp:4
	v_mfma_f32_16x16x128_f8f6f4 v[74:77], v[222:225], v[210:213], v[74:77] cbsz:4 blgp:4
	v_mfma_f32_16x16x128_f8f6f4 v[78:81], v[218:221], v[202:205], v[78:81] cbsz:4 blgp:4
	v_mfma_f32_16x16x128_f8f6f4 v[78:81], v[226:229], v[210:213], v[78:81] cbsz:4 blgp:4
	s_barrier
	s_mov_b32 m0, s62
	s_nop 0
	global_load_lds_dwordx4 v164, s[40:41]
	s_mov_b32 m0, s63
	s_nop 0
	global_load_lds_dwordx4 v168, s[40:41]
	ds_read_b128 v[182:185], v179 offset:49152
	ds_read_b128 v[186:189], v179 offset:51200
	ds_read_b128 v[190:193], v180 offset:49152
	ds_read_b128 v[194:197], v180 offset:51200
	ds_read_b128 v[198:201], v179 offset:53248
	ds_read_b128 v[202:205], v179 offset:55296
	ds_read_b128 v[206:209], v180 offset:53248
	ds_read_b128 v[210:213], v180 offset:55296
	s_mov_b32 m0, s64
	s_nop 0
	global_load_lds_dwordx4 v162, s[42:43]
	s_mov_b32 m0, s65
	s_nop 0
	global_load_lds_dwordx4 v166, s[42:43]
	s_add_u32 s40, s40, s22
	s_addc_u32 s41, s41, s23
	s_mov_b32 m0, s66
	s_nop 0
	global_load_lds_dwordx4 v164, s[40:41]
	s_mov_b32 m0, s67
	s_nop 0
	global_load_lds_dwordx4 v168, s[40:41]
	s_waitcnt vmcnt(8)
	s_waitcnt lgkmcnt(0)
	s_barrier
	v_mfma_f32_16x16x128_f8f6f4 v[86:89], v[146:149], v[182:185], v[86:89] cbsz:4 blgp:4
	v_mfma_f32_16x16x128_f8f6f4 v[86:89], v[154:157], v[190:193], v[86:89] cbsz:4 blgp:4
	v_mfma_f32_16x16x128_f8f6f4 v[90:93], v[150:153], v[182:185], v[90:93] cbsz:4 blgp:4
	v_mfma_f32_16x16x128_f8f6f4 v[90:93], v[158:161], v[190:193], v[90:93] cbsz:4 blgp:4
	v_mfma_f32_16x16x128_f8f6f4 v[98:101], v[146:149], v[186:189], v[98:101] cbsz:4 blgp:4
	v_mfma_f32_16x16x128_f8f6f4 v[98:101], v[154:157], v[194:197], v[98:101] cbsz:4 blgp:4
	v_mfma_f32_16x16x128_f8f6f4 v[106:109], v[150:153], v[186:189], v[106:109] cbsz:4 blgp:4
	v_mfma_f32_16x16x128_f8f6f4 v[106:109], v[158:161], v[194:197], v[106:109] cbsz:4 blgp:4
	v_mfma_f32_16x16x128_f8f6f4 v[118:121], v[146:149], v[198:201], v[118:121] cbsz:4 blgp:4
	v_mfma_f32_16x16x128_f8f6f4 v[118:121], v[154:157], v[206:209], v[118:121] cbsz:4 blgp:4
	v_mfma_f32_16x16x128_f8f6f4 v[126:129], v[150:153], v[198:201], v[126:129] cbsz:4 blgp:4
	v_mfma_f32_16x16x128_f8f6f4 v[126:129], v[158:161], v[206:209], v[126:129] cbsz:4 blgp:4
	v_mfma_f32_16x16x128_f8f6f4 v[138:141], v[146:149], v[202:205], v[138:141] cbsz:4 blgp:4
	v_mfma_f32_16x16x128_f8f6f4 v[138:141], v[154:157], v[210:213], v[138:141] cbsz:4 blgp:4
	v_mfma_f32_16x16x128_f8f6f4 v[82:85], v[150:153], v[202:205], v[82:85] cbsz:4 blgp:4
	v_mfma_f32_16x16x128_f8f6f4 v[82:85], v[158:161], v[210:213], v[82:85] cbsz:4 blgp:4
	v_mfma_f32_16x16x128_f8f6f4 v[94:97], v[214:217], v[182:185], v[94:97] cbsz:4 blgp:4
	v_mfma_f32_16x16x128_f8f6f4 v[94:97], v[222:225], v[190:193], v[94:97] cbsz:4 blgp:4
	v_mfma_f32_16x16x128_f8f6f4 v[102:105], v[218:221], v[182:185], v[102:105] cbsz:4 blgp:4
	v_mfma_f32_16x16x128_f8f6f4 v[102:105], v[226:229], v[190:193], v[102:105] cbsz:4 blgp:4
	v_mfma_f32_16x16x128_f8f6f4 v[110:113], v[214:217], v[186:189], v[110:113] cbsz:4 blgp:4
	v_mfma_f32_16x16x128_f8f6f4 v[110:113], v[222:225], v[194:197], v[110:113] cbsz:4 blgp:4
	v_mfma_f32_16x16x128_f8f6f4 v[114:117], v[218:221], v[186:189], v[114:117] cbsz:4 blgp:4
	v_mfma_f32_16x16x128_f8f6f4 v[114:117], v[226:229], v[194:197], v[114:117] cbsz:4 blgp:4
	v_mfma_f32_16x16x128_f8f6f4 v[122:125], v[214:217], v[198:201], v[122:125] cbsz:4 blgp:4
	v_mfma_f32_16x16x128_f8f6f4 v[122:125], v[222:225], v[206:209], v[122:125] cbsz:4 blgp:4
	v_mfma_f32_16x16x128_f8f6f4 v[130:133], v[218:221], v[198:201], v[130:133] cbsz:4 blgp:4
	v_mfma_f32_16x16x128_f8f6f4 v[130:133], v[226:229], v[206:209], v[130:133] cbsz:4 blgp:4
	v_mfma_f32_16x16x128_f8f6f4 v[134:137], v[214:217], v[202:205], v[134:137] cbsz:4 blgp:4
	v_mfma_f32_16x16x128_f8f6f4 v[134:137], v[222:225], v[210:213], v[134:137] cbsz:4 blgp:4
	v_mfma_f32_16x16x128_f8f6f4 v[142:145], v[218:221], v[202:205], v[142:145] cbsz:4 blgp:4
	v_mfma_f32_16x16x128_f8f6f4 v[142:145], v[226:229], v[210:213], v[142:145] cbsz:4 blgp:4
	s_andn2_b64 vcc, exec, s[28:29]
	s_barrier
	s_cbranch_vccnz .LBB6_20
	s_ashr_i32 s39, s38, 31
	s_lshl_b64 s[38:39], s[38:39], 10
	s_add_u32 s38, s14, s38
	s_addc_u32 s39, s15, s39
	s_add_u32 s31, s36, 0x200
	s_addc_u32 s46, s37, 0
	s_add_u32 s47, s34, 0x200
	s_addc_u32 s81, s35, 0
	s_add_u32 s34, s82, 0x180
	s_addc_u32 s35, s83, 0
	s_mov_b32 s82, 4
	s_cmp_eq_u32 s61, s82
	s_cselect_b64 s[36:37], -1, 0
	s_cmp_lg_u32 s61, s82
	s_cbranch_scc1 .LBB6_18

.LBB6_18:
	ds_read_b128 v[146:149], v169
	ds_read_b128 v[150:153], v169 offset:2048
	ds_read_b128 v[154:157], v178
	ds_read_b128 v[158:161], v178 offset:2048
	s_and_b64 s[36:37], s[36:37], exec
	s_cselect_b32 s42, s4, s31
	s_cselect_b32 s43, s5, s46
	s_cselect_b32 s45, s7, s81
	s_cselect_b32 s44, s6, s47
	s_add_u32 s40, s42, 0x80
	s_addc_u32 s41, s43, 0
	s_add_u32 s36, s44, 0x80
	s_addc_u32 s37, s45, 0
	ds_read_b128 v[182:185], v179
	ds_read_b128 v[186:189], v179 offset:2048
	ds_read_b128 v[190:193], v180
	ds_read_b128 v[194:197], v180 offset:2048
	ds_read_b128 v[198:201], v179 offset:4096
	ds_read_b128 v[202:205], v179 offset:6144
	ds_read_b128 v[206:209], v180 offset:4096
	ds_read_b128 v[210:213], v180 offset:6144
	s_mov_b32 m0, s68
	s_nop 0
	global_load_lds_dwordx4 v162, s[34:35]
	s_mov_b32 m0, s69
	s_nop 0
	global_load_lds_dwordx4 v166, s[34:35]
	s_waitcnt lgkmcnt(8)
	ds_read_b128 v[214:217], v169 offset:16384
	ds_read_b128 v[218:221], v169 offset:18432
	ds_read_b128 v[222:225], v178 offset:16384
	ds_read_b128 v[226:229], v178 offset:18432
	s_waitcnt vmcnt(8)
	s_waitcnt lgkmcnt(0)
	s_barrier
	s_waitcnt lgkmcnt(0)
	v_mfma_f32_16x16x128_f8f6f4 v[18:21], v[146:149], v[182:185], v[18:21] cbsz:4 blgp:4
	v_mfma_f32_16x16x128_f8f6f4 v[18:21], v[154:157], v[190:193], v[18:21] cbsz:4 blgp:4
	v_mfma_f32_16x16x128_f8f6f4 v[22:25], v[150:153], v[182:185], v[22:25] cbsz:4 blgp:4
	v_mfma_f32_16x16x128_f8f6f4 v[22:25], v[158:161], v[190:193], v[22:25] cbsz:4 blgp:4
	v_mfma_f32_16x16x128_f8f6f4 v[26:29], v[146:149], v[186:189], v[26:29] cbsz:4 blgp:4
	v_mfma_f32_16x16x128_f8f6f4 v[26:29], v[154:157], v[194:197], v[26:29] cbsz:4 blgp:4
	v_mfma_f32_16x16x128_f8f6f4 v[30:33], v[150:153], v[186:189], v[30:33] cbsz:4 blgp:4
	v_mfma_f32_16x16x128_f8f6f4 v[30:33], v[158:161], v[194:197], v[30:33] cbsz:4 blgp:4
	v_mfma_f32_16x16x128_f8f6f4 v[34:37], v[146:149], v[198:201], v[34:37] cbsz:4 blgp:4
	v_mfma_f32_16x16x128_f8f6f4 v[34:37], v[154:157], v[206:209], v[34:37] cbsz:4 blgp:4
	v_mfma_f32_16x16x128_f8f6f4 v[38:41], v[150:153], v[198:201], v[38:41] cbsz:4 blgp:4
	v_mfma_f32_16x16x128_f8f6f4 v[38:41], v[158:161], v[206:209], v[38:41] cbsz:4 blgp:4
	v_mfma_f32_16x16x128_f8f6f4 v[42:45], v[146:149], v[202:205], v[42:45] cbsz:4 blgp:4
	v_mfma_f32_16x16x128_f8f6f4 v[42:45], v[154:157], v[210:213], v[42:45] cbsz:4 blgp:4
	v_mfma_f32_16x16x128_f8f6f4 v[46:49], v[150:153], v[202:205], v[46:49] cbsz:4 blgp:4
	v_mfma_f32_16x16x128_f8f6f4 v[46:49], v[158:161], v[210:213], v[46:49] cbsz:4 blgp:4
	v_mfma_f32_16x16x128_f8f6f4 v[50:53], v[214:217], v[182:185], v[50:53] cbsz:4 blgp:4
	v_mfma_f32_16x16x128_f8f6f4 v[50:53], v[222:225], v[190:193], v[50:53] cbsz:4 blgp:4
	v_mfma_f32_16x16x128_f8f6f4 v[54:57], v[218:221], v[182:185], v[54:57] cbsz:4 blgp:4
	v_mfma_f32_16x16x128_f8f6f4 v[54:57], v[226:229], v[190:193], v[54:57] cbsz:4 blgp:4
	v_mfma_f32_16x16x128_f8f6f4 v[58:61], v[214:217], v[186:189], v[58:61] cbsz:4 blgp:4
	v_mfma_f32_16x16x128_f8f6f4 v[58:61], v[222:225], v[194:197], v[58:61] cbsz:4 blgp:4
	v_mfma_f32_16x16x128_f8f6f4 v[62:65], v[218:221], v[186:189], v[62:65] cbsz:4 blgp:4
	v_mfma_f32_16x16x128_f8f6f4 v[62:65], v[226:229], v[194:197], v[62:65] cbsz:4 blgp:4
	v_mfma_f32_16x16x128_f8f6f4 v[66:69], v[214:217], v[198:201], v[66:69] cbsz:4 blgp:4
	v_mfma_f32_16x16x128_f8f6f4 v[66:69], v[222:225], v[206:209], v[66:69] cbsz:4 blgp:4
	v_mfma_f32_16x16x128_f8f6f4 v[70:73], v[218:221], v[198:201], v[70:73] cbsz:4 blgp:4
	v_mfma_f32_16x16x128_f8f6f4 v[70:73], v[226:229], v[206:209], v[70:73] cbsz:4 blgp:4
	v_mfma_f32_16x16x128_f8f6f4 v[74:77], v[214:217], v[202:205], v[74:77] cbsz:4 blgp:4
	v_mfma_f32_16x16x128_f8f6f4 v[74:77], v[222:225], v[210:213], v[74:77] cbsz:4 blgp:4
	v_mfma_f32_16x16x128_f8f6f4 v[78:81], v[218:221], v[202:205], v[78:81] cbsz:4 blgp:4
	v_mfma_f32_16x16x128_f8f6f4 v[78:81], v[226:229], v[210:213], v[78:81] cbsz:4 blgp:4
	s_barrier
	s_mov_b32 m0, s54
	s_nop 0
	global_load_lds_dwordx4 v164, s[44:45]
	s_mov_b32 m0, s55
	s_nop 0
	global_load_lds_dwordx4 v168, s[44:45]
	ds_read_b128 v[182:185], v179 offset:16384
	ds_read_b128 v[186:189], v179 offset:18432
	ds_read_b128 v[190:193], v180 offset:16384
	ds_read_b128 v[194:197], v180 offset:18432
	ds_read_b128 v[198:201], v179 offset:20480
	ds_read_b128 v[202:205], v179 offset:22528
	ds_read_b128 v[206:209], v180 offset:20480
	ds_read_b128 v[210:213], v180 offset:22528
	s_mov_b32 m0, s53
	s_nop 0
	global_load_lds_dwordx4 v162, s[42:43]
	s_mov_b32 m0, s56
	s_nop 0
	global_load_lds_dwordx4 v166, s[42:43]
	s_add_u32 s44, s44, s22
	s_addc_u32 s45, s45, s23
	s_mov_b32 m0, s57
	s_nop 0
	global_load_lds_dwordx4 v164, s[44:45]
	s_mov_b32 m0, s58
	s_nop 0
	global_load_lds_dwordx4 v168, s[44:45]
	s_waitcnt vmcnt(8)
	s_waitcnt lgkmcnt(0)
	s_barrier
	v_mfma_f32_16x16x128_f8f6f4 v[86:89], v[146:149], v[182:185], v[86:89] cbsz:4 blgp:4
	v_mfma_f32_16x16x128_f8f6f4 v[86:89], v[154:157], v[190:193], v[86:89] cbsz:4 blgp:4
	v_mfma_f32_16x16x128_f8f6f4 v[90:93], v[150:153], v[182:185], v[90:93] cbsz:4 blgp:4
	v_mfma_f32_16x16x128_f8f6f4 v[90:93], v[158:161], v[190:193], v[90:93] cbsz:4 blgp:4
	v_mfma_f32_16x16x128_f8f6f4 v[98:101], v[146:149], v[186:189], v[98:101] cbsz:4 blgp:4
	v_mfma_f32_16x16x128_f8f6f4 v[98:101], v[154:157], v[194:197], v[98:101] cbsz:4 blgp:4
	v_mfma_f32_16x16x128_f8f6f4 v[106:109], v[150:153], v[186:189], v[106:109] cbsz:4 blgp:4
	v_mfma_f32_16x16x128_f8f6f4 v[106:109], v[158:161], v[194:197], v[106:109] cbsz:4 blgp:4
	v_mfma_f32_16x16x128_f8f6f4 v[118:121], v[146:149], v[198:201], v[118:121] cbsz:4 blgp:4
	v_mfma_f32_16x16x128_f8f6f4 v[118:121], v[154:157], v[206:209], v[118:121] cbsz:4 blgp:4
	v_mfma_f32_16x16x128_f8f6f4 v[126:129], v[150:153], v[198:201], v[126:129] cbsz:4 blgp:4
	v_mfma_f32_16x16x128_f8f6f4 v[126:129], v[158:161], v[206:209], v[126:129] cbsz:4 blgp:4
	v_mfma_f32_16x16x128_f8f6f4 v[138:141], v[146:149], v[202:205], v[138:141] cbsz:4 blgp:4
	v_mfma_f32_16x16x128_f8f6f4 v[138:141], v[154:157], v[210:213], v[138:141] cbsz:4 blgp:4
	v_mfma_f32_16x16x128_f8f6f4 v[82:85], v[150:153], v[202:205], v[82:85] cbsz:4 blgp:4
	v_mfma_f32_16x16x128_f8f6f4 v[82:85], v[158:161], v[210:213], v[82:85] cbsz:4 blgp:4
	v_mfma_f32_16x16x128_f8f6f4 v[94:97], v[214:217], v[182:185], v[94:97] cbsz:4 blgp:4
	v_mfma_f32_16x16x128_f8f6f4 v[94:97], v[222:225], v[190:193], v[94:97] cbsz:4 blgp:4
	v_mfma_f32_16x16x128_f8f6f4 v[102:105], v[218:221], v[182:185], v[102:105] cbsz:4 blgp:4
	v_mfma_f32_16x16x128_f8f6f4 v[102:105], v[226:229], v[190:193], v[102:105] cbsz:4 blgp:4
	v_mfma_f32_16x16x128_f8f6f4 v[110:113], v[214:217], v[186:189], v[110:113] cbsz:4 blgp:4
	v_mfma_f32_16x16x128_f8f6f4 v[110:113], v[222:225], v[194:197], v[110:113] cbsz:4 blgp:4
	v_mfma_f32_16x16x128_f8f6f4 v[114:117], v[218:221], v[186:189], v[114:117] cbsz:4 blgp:4
	v_mfma_f32_16x16x128_f8f6f4 v[114:117], v[226:229], v[194:197], v[114:117] cbsz:4 blgp:4
	v_mfma_f32_16x16x128_f8f6f4 v[122:125], v[214:217], v[198:201], v[122:125] cbsz:4 blgp:4
	v_mfma_f32_16x16x128_f8f6f4 v[122:125], v[222:225], v[206:209], v[122:125] cbsz:4 blgp:4
	v_mfma_f32_16x16x128_f8f6f4 v[130:133], v[218:221], v[198:201], v[130:133] cbsz:4 blgp:4
	v_mfma_f32_16x16x128_f8f6f4 v[130:133], v[226:229], v[206:209], v[130:133] cbsz:4 blgp:4
	v_mfma_f32_16x16x128_f8f6f4 v[134:137], v[214:217], v[202:205], v[134:137] cbsz:4 blgp:4
	v_mfma_f32_16x16x128_f8f6f4 v[134:137], v[222:225], v[210:213], v[134:137] cbsz:4 blgp:4
	v_mfma_f32_16x16x128_f8f6f4 v[142:145], v[218:221], v[202:205], v[142:145] cbsz:4 blgp:4
	v_mfma_f32_16x16x128_f8f6f4 v[142:145], v[226:229], v[210:213], v[142:145] cbsz:4 blgp:4
	s_barrier
	ds_read_b128 v[146:149], v169 offset:32768
	ds_read_b128 v[150:153], v169 offset:34816
	ds_read_b128 v[154:157], v178 offset:32768
	ds_read_b128 v[158:161], v178 offset:34816
	ds_read_b128 v[182:185], v179 offset:32768
	ds_read_b128 v[186:189], v179 offset:34816
	ds_read_b128 v[190:193], v180 offset:32768
	ds_read_b128 v[194:197], v180 offset:34816
	ds_read_b128 v[198:201], v179 offset:36864
	ds_read_b128 v[202:205], v179 offset:38912
	ds_read_b128 v[206:209], v180 offset:36864
	ds_read_b128 v[210:213], v180 offset:38912
	s_add_u32 s42, s42, s20
	s_addc_u32 s43, s43, s21
	s_mov_b32 m0, s59
	s_nop 0
	global_load_lds_dwordx4 v162, s[42:43]
	s_mov_b32 m0, s60
	s_nop 0
	global_load_lds_dwordx4 v166, s[42:43]
	s_waitcnt lgkmcnt(8)
	ds_read_b128 v[214:217], v169 offset:49152
	ds_read_b128 v[218:221], v169 offset:51200
	ds_read_b128 v[222:225], v178 offset:49152
	ds_read_b128 v[226:229], v178 offset:51200
	s_waitcnt vmcnt(8)
	s_waitcnt lgkmcnt(0)
	s_barrier
	s_waitcnt lgkmcnt(0)
	v_mfma_f32_16x16x128_f8f6f4 v[18:21], v[146:149], v[182:185], v[18:21] cbsz:4 blgp:4
	v_mfma_f32_16x16x128_f8f6f4 v[18:21], v[154:157], v[190:193], v[18:21] cbsz:4 blgp:4
	v_mfma_f32_16x16x128_f8f6f4 v[22:25], v[150:153], v[182:185], v[22:25] cbsz:4 blgp:4
	v_mfma_f32_16x16x128_f8f6f4 v[22:25], v[158:161], v[190:193], v[22:25] cbsz:4 blgp:4
	v_mfma_f32_16x16x128_f8f6f4 v[26:29], v[146:149], v[186:189], v[26:29] cbsz:4 blgp:4
	v_mfma_f32_16x16x128_f8f6f4 v[26:29], v[154:157], v[194:197], v[26:29] cbsz:4 blgp:4
	v_mfma_f32_16x16x128_f8f6f4 v[30:33], v[150:153], v[186:189], v[30:33] cbsz:4 blgp:4
	v_mfma_f32_16x16x128_f8f6f4 v[30:33], v[158:161], v[194:197], v[30:33] cbsz:4 blgp:4
	v_mfma_f32_16x16x128_f8f6f4 v[34:37], v[146:149], v[198:201], v[34:37] cbsz:4 blgp:4
	v_mfma_f32_16x16x128_f8f6f4 v[34:37], v[154:157], v[206:209], v[34:37] cbsz:4 blgp:4
	v_mfma_f32_16x16x128_f8f6f4 v[38:41], v[150:153], v[198:201], v[38:41] cbsz:4 blgp:4
	v_mfma_f32_16x16x128_f8f6f4 v[38:41], v[158:161], v[206:209], v[38:41] cbsz:4 blgp:4
	v_mfma_f32_16x16x128_f8f6f4 v[42:45], v[146:149], v[202:205], v[42:45] cbsz:4 blgp:4
	v_mfma_f32_16x16x128_f8f6f4 v[42:45], v[154:157], v[210:213], v[42:45] cbsz:4 blgp:4
	v_mfma_f32_16x16x128_f8f6f4 v[46:49], v[150:153], v[202:205], v[46:49] cbsz:4 blgp:4
	v_mfma_f32_16x16x128_f8f6f4 v[46:49], v[158:161], v[210:213], v[46:49] cbsz:4 blgp:4
	v_mfma_f32_16x16x128_f8f6f4 v[50:53], v[214:217], v[182:185], v[50:53] cbsz:4 blgp:4
	v_mfma_f32_16x16x128_f8f6f4 v[50:53], v[222:225], v[190:193], v[50:53] cbsz:4 blgp:4
	v_mfma_f32_16x16x128_f8f6f4 v[54:57], v[218:221], v[182:185], v[54:57] cbsz:4 blgp:4
	v_mfma_f32_16x16x128_f8f6f4 v[54:57], v[226:229], v[190:193], v[54:57] cbsz:4 blgp:4
	v_mfma_f32_16x16x128_f8f6f4 v[58:61], v[214:217], v[186:189], v[58:61] cbsz:4 blgp:4
	v_mfma_f32_16x16x128_f8f6f4 v[58:61], v[222:225], v[194:197], v[58:61] cbsz:4 blgp:4
	v_mfma_f32_16x16x128_f8f6f4 v[62:65], v[218:221], v[186:189], v[62:65] cbsz:4 blgp:4
	v_mfma_f32_16x16x128_f8f6f4 v[62:65], v[226:229], v[194:197], v[62:65] cbsz:4 blgp:4
	v_mfma_f32_16x16x128_f8f6f4 v[66:69], v[214:217], v[198:201], v[66:69] cbsz:4 blgp:4
	v_mfma_f32_16x16x128_f8f6f4 v[66:69], v[222:225], v[206:209], v[66:69] cbsz:4 blgp:4
	v_mfma_f32_16x16x128_f8f6f4 v[70:73], v[218:221], v[198:201], v[70:73] cbsz:4 blgp:4
	v_mfma_f32_16x16x128_f8f6f4 v[70:73], v[226:229], v[206:209], v[70:73] cbsz:4 blgp:4
	v_mfma_f32_16x16x128_f8f6f4 v[74:77], v[214:217], v[202:205], v[74:77] cbsz:4 blgp:4
	v_mfma_f32_16x16x128_f8f6f4 v[74:77], v[222:225], v[210:213], v[74:77] cbsz:4 blgp:4
	v_mfma_f32_16x16x128_f8f6f4 v[78:81], v[218:221], v[202:205], v[78:81] cbsz:4 blgp:4
	v_mfma_f32_16x16x128_f8f6f4 v[78:81], v[226:229], v[210:213], v[78:81] cbsz:4 blgp:4
	s_barrier
	s_mov_b32 m0, s62
	s_nop 0
	global_load_lds_dwordx4 v164, s[36:37]
	s_mov_b32 m0, s63
	s_nop 0
	global_load_lds_dwordx4 v168, s[36:37]
	ds_read_b128 v[182:185], v179 offset:49152
	ds_read_b128 v[186:189], v179 offset:51200
	ds_read_b128 v[190:193], v180 offset:49152
	ds_read_b128 v[194:197], v180 offset:51200
	ds_read_b128 v[198:201], v179 offset:53248
	ds_read_b128 v[202:205], v179 offset:55296
	ds_read_b128 v[206:209], v180 offset:53248
	ds_read_b128 v[210:213], v180 offset:55296
	s_mov_b32 m0, s64
	s_nop 0
	global_load_lds_dwordx4 v162, s[40:41]
	s_mov_b32 m0, s65
	s_nop 0
	global_load_lds_dwordx4 v166, s[40:41]
	s_add_u32 s36, s36, s22
	s_addc_u32 s37, s37, s23
	s_mov_b32 m0, s66
	s_nop 0
	global_load_lds_dwordx4 v164, s[36:37]
	s_mov_b32 m0, s67
	s_nop 0
	global_load_lds_dwordx4 v168, s[36:37]
	s_waitcnt vmcnt(8)
	s_waitcnt lgkmcnt(0)
	s_barrier
	v_mfma_f32_16x16x128_f8f6f4 v[86:89], v[146:149], v[182:185], v[86:89] cbsz:4 blgp:4
	v_mfma_f32_16x16x128_f8f6f4 v[86:89], v[154:157], v[190:193], v[86:89] cbsz:4 blgp:4
	v_mfma_f32_16x16x128_f8f6f4 v[90:93], v[150:153], v[182:185], v[90:93] cbsz:4 blgp:4
	v_mfma_f32_16x16x128_f8f6f4 v[90:93], v[158:161], v[190:193], v[90:93] cbsz:4 blgp:4
	v_mfma_f32_16x16x128_f8f6f4 v[98:101], v[146:149], v[186:189], v[98:101] cbsz:4 blgp:4
	v_mfma_f32_16x16x128_f8f6f4 v[98:101], v[154:157], v[194:197], v[98:101] cbsz:4 blgp:4
	v_mfma_f32_16x16x128_f8f6f4 v[106:109], v[150:153], v[186:189], v[106:109] cbsz:4 blgp:4
	v_mfma_f32_16x16x128_f8f6f4 v[106:109], v[158:161], v[194:197], v[106:109] cbsz:4 blgp:4
	v_mfma_f32_16x16x128_f8f6f4 v[118:121], v[146:149], v[198:201], v[118:121] cbsz:4 blgp:4
	v_mfma_f32_16x16x128_f8f6f4 v[118:121], v[154:157], v[206:209], v[118:121] cbsz:4 blgp:4
	v_mfma_f32_16x16x128_f8f6f4 v[126:129], v[150:153], v[198:201], v[126:129] cbsz:4 blgp:4
	v_mfma_f32_16x16x128_f8f6f4 v[126:129], v[158:161], v[206:209], v[126:129] cbsz:4 blgp:4
	v_mfma_f32_16x16x128_f8f6f4 v[138:141], v[146:149], v[202:205], v[138:141] cbsz:4 blgp:4
	v_mfma_f32_16x16x128_f8f6f4 v[138:141], v[154:157], v[210:213], v[138:141] cbsz:4 blgp:4
	v_mfma_f32_16x16x128_f8f6f4 v[82:85], v[150:153], v[202:205], v[82:85] cbsz:4 blgp:4
	v_mfma_f32_16x16x128_f8f6f4 v[82:85], v[158:161], v[210:213], v[82:85] cbsz:4 blgp:4
	v_mfma_f32_16x16x128_f8f6f4 v[94:97], v[214:217], v[182:185], v[94:97] cbsz:4 blgp:4
	v_mfma_f32_16x16x128_f8f6f4 v[94:97], v[222:225], v[190:193], v[94:97] cbsz:4 blgp:4
	v_mfma_f32_16x16x128_f8f6f4 v[102:105], v[218:221], v[182:185], v[102:105] cbsz:4 blgp:4
	v_mfma_f32_16x16x128_f8f6f4 v[102:105], v[226:229], v[190:193], v[102:105] cbsz:4 blgp:4
	v_mfma_f32_16x16x128_f8f6f4 v[110:113], v[214:217], v[186:189], v[110:113] cbsz:4 blgp:4
	v_mfma_f32_16x16x128_f8f6f4 v[110:113], v[222:225], v[194:197], v[110:113] cbsz:4 blgp:4
	v_mfma_f32_16x16x128_f8f6f4 v[114:117], v[218:221], v[186:189], v[114:117] cbsz:4 blgp:4
	v_mfma_f32_16x16x128_f8f6f4 v[114:117], v[226:229], v[194:197], v[114:117] cbsz:4 blgp:4
	v_mfma_f32_16x16x128_f8f6f4 v[122:125], v[214:217], v[198:201], v[122:125] cbsz:4 blgp:4
	v_mfma_f32_16x16x128_f8f6f4 v[122:125], v[222:225], v[206:209], v[122:125] cbsz:4 blgp:4
	v_mfma_f32_16x16x128_f8f6f4 v[130:133], v[218:221], v[198:201], v[130:133] cbsz:4 blgp:4
	v_mfma_f32_16x16x128_f8f6f4 v[130:133], v[226:229], v[206:209], v[130:133] cbsz:4 blgp:4
	v_mfma_f32_16x16x128_f8f6f4 v[134:137], v[214:217], v[202:205], v[134:137] cbsz:4 blgp:4
	v_mfma_f32_16x16x128_f8f6f4 v[134:137], v[222:225], v[210:213], v[134:137] cbsz:4 blgp:4
	v_mfma_f32_16x16x128_f8f6f4 v[142:145], v[218:221], v[202:205], v[142:145] cbsz:4 blgp:4
	v_mfma_f32_16x16x128_f8f6f4 v[142:145], v[226:229], v[210:213], v[142:145] cbsz:4 blgp:4
	s_add_i32 s36, s82, 2
	s_add_u32 s31, s31, 0x100
	s_addc_u32 s46, s46, 0
	s_add_u32 s47, s47, 0x100
	s_addc_u32 s81, s81, 0
	s_add_u32 s34, s34, 0x100
	s_addc_u32 s35, s35, 0
	s_cmp_ge_i32 s82, s61
	s_barrier
	s_cbranch_scc1 .LBB6_20
	s_mov_b32 s82, s36
	s_cmp_eq_u32 s61, s82
	s_cselect_b64 s[36:37], -1, 0
	s_cmp_lg_u32 s61, s82
	s_cbranch_scc0 .LBB6_17
	s_branch .LBB6_18
